# prep: gate blocks write the fp16 copy of x from their MFMA operands, the 1024 x-convert blocks exit at once (x read once)
# speedup vs baseline: 1.0053x; 1.0053x over previous
.LBB13_3:
	s_cmpk_lt_i32 s2, 0x500
	v_lshrrev_b32_e32 v1, 6, v0
	v_and_b32_e32 v36, 63, v0
	s_cbranch_scc0 .LBB13_5
	v_bfe_u32 v13, v0, 4, 2
	v_and_b32_e32 v12, 15, v0
	s_lshl_b32 s22, s2, 4
	v_lshlrev_b32_e32 v2, 3, v13
	v_lshl_or_b32 v14, v1, 8, v2
	v_or_b32_e32 v2, s22, v12
	s_load_dwordx8 s[4:11], s[0:1], 0x30
	s_load_dwordx2 s[26:27], s[0:1], 0x60
	v_ashrrev_i32_e32 v3, 31, v2
	v_lshlrev_b64 v[2:3], 12, v[2:3]
	s_waitcnt lgkmcnt(0)
	v_lshl_add_u64 v[2:3], s[20:21], 0, v[2:3]
	v_lshlrev_b32_e32 v18, 2, v14
	v_mov_b32_e32 v19, 0
	v_lshl_or_b32 v14, v14, 4, v12
	v_lshl_add_u64 v[10:11], v[2:3], 0, v[18:19]
	v_subrev_u32_e32 v108, s20, v10
	v_lshrrev_b32_e32 v108, 1, v108
	v_or_b32_e32 v18, 0x200, v14
	v_lshlrev_b64 v[16:17], 2, v[18:19]
	v_lshlrev_b32_e32 v15, 2, v14
	v_lshl_add_u64 v[28:29], s[4:5], 0, v[16:17]
	v_lshl_add_u64 v[16:17], s[10:11], 0, v[16:17]
	v_or_b32_e32 v18, 0x400, v14
	global_load_dwordx4 v[2:5], v[10:11], off offset:16
	global_load_dwordx4 v[6:9], v[10:11], off
	global_load_dword v37, v15, s[4:5]
	global_load_dword v48, v15, s[10:11]
	global_load_dword v49, v15, s[4:5] offset:64
	global_load_dword v50, v15, s[10:11] offset:64
	global_load_dword v51, v15, s[4:5] offset:128
	global_load_dword v52, v15, s[10:11] offset:128
	global_load_dword v53, v15, s[4:5] offset:192
	global_load_dword v54, v15, s[10:11] offset:192
	global_load_dword v55, v15, s[4:5] offset:256
	global_load_dword v56, v15, s[10:11] offset:256
	global_load_dword v57, v15, s[4:5] offset:320
	global_load_dword v58, v15, s[10:11] offset:320
	global_load_dword v59, v15, s[4:5] offset:384
	global_load_dword v60, v15, s[10:11] offset:384
	global_load_dword v61, v15, s[4:5] offset:448
	global_load_dword v62, v15, s[10:11] offset:448
	global_load_dwordx4 v[20:23], v[10:11], off offset:144
	global_load_dwordx4 v[24:27], v[10:11], off offset:128
	global_load_dword v63, v[28:29], off
	global_load_dword v64, v[16:17], off
	global_load_dword v65, v15, s[4:5] offset:2112
	global_load_dword v66, v15, s[10:11] offset:2112
	global_load_dword v67, v15, s[4:5] offset:2176
	global_load_dword v68, v15, s[10:11] offset:2176
	global_load_dword v69, v15, s[4:5] offset:2240
	global_load_dword v70, v15, s[10:11] offset:2240
	global_load_dword v71, v15, s[4:5] offset:2304
	global_load_dword v72, v15, s[10:11] offset:2304
	global_load_dword v73, v15, s[4:5] offset:2368
	global_load_dword v74, v15, s[10:11] offset:2368
	global_load_dword v75, v15, s[4:5] offset:2432
	global_load_dword v76, v15, s[10:11] offset:2432
	global_load_dword v77, v15, s[4:5] offset:2496
	global_load_dword v78, v15, s[10:11] offset:2496
	s_nop 0
	global_load_dwordx4 v[28:31], v[10:11], off offset:272
	global_load_dwordx4 v[32:35], v[10:11], off offset:256
	v_lshlrev_b64 v[16:17], 2, v[18:19]
	v_lshl_add_u64 v[38:39], s[4:5], 0, v[16:17]
	v_lshl_add_u64 v[16:17], s[10:11], 0, v[16:17]
	v_or_b32_e32 v18, 0x410, v14
	global_load_dword v79, v[16:17], off
	v_lshlrev_b64 v[16:17], 2, v[18:19]
	global_load_dword v15, v[38:39], off
	v_lshl_add_u64 v[38:39], s[4:5], 0, v[16:17]
	v_lshl_add_u64 v[16:17], s[10:11], 0, v[16:17]
	v_or_b32_e32 v18, 0x420, v14
	global_load_dword v81, v[16:17], off
	v_lshlrev_b64 v[16:17], 2, v[18:19]
	global_load_dword v80, v[38:39], off
	v_lshl_add_u64 v[38:39], s[4:5], 0, v[16:17]
	v_lshl_add_u64 v[16:17], s[10:11], 0, v[16:17]
	v_or_b32_e32 v18, 0x430, v14
	global_load_dword v83, v[16:17], off
	v_lshlrev_b64 v[16:17], 2, v[18:19]
	global_load_dword v82, v[38:39], off
	v_lshl_add_u64 v[38:39], s[4:5], 0, v[16:17]
	v_lshl_add_u64 v[16:17], s[10:11], 0, v[16:17]
	v_or_b32_e32 v18, 0x440, v14
	global_load_dword v85, v[16:17], off
	v_lshlrev_b64 v[16:17], 2, v[18:19]
	global_load_dword v84, v[38:39], off
	v_lshl_add_u64 v[38:39], s[4:5], 0, v[16:17]
	v_lshl_add_u64 v[16:17], s[10:11], 0, v[16:17]
	v_or_b32_e32 v18, 0x450, v14
	global_load_dword v87, v[16:17], off
	v_lshlrev_b64 v[16:17], 2, v[18:19]
	global_load_dword v86, v[38:39], off
	v_lshl_add_u64 v[38:39], s[4:5], 0, v[16:17]
	v_lshl_add_u64 v[16:17], s[10:11], 0, v[16:17]
	v_or_b32_e32 v18, 0x460, v14
	global_load_dword v89, v[16:17], off
	v_lshlrev_b64 v[16:17], 2, v[18:19]
	global_load_dword v88, v[38:39], off
	v_lshl_add_u64 v[38:39], s[4:5], 0, v[16:17]
	v_lshl_add_u64 v[16:17], s[10:11], 0, v[16:17]
	v_or_b32_e32 v18, 0x470, v14
	global_load_dword v91, v[16:17], off
	v_lshlrev_b64 v[16:17], 2, v[18:19]
	global_load_dword v90, v[38:39], off
	v_lshl_add_u64 v[38:39], s[4:5], 0, v[16:17]
	v_lshl_add_u64 v[16:17], s[10:11], 0, v[16:17]
	v_or_b32_e32 v18, 0x600, v14
	global_load_dword v92, v[38:39], off
	global_load_dword v93, v[16:17], off
	s_nop 0
	global_load_dwordx4 v[38:41], v[10:11], off offset:400
	global_load_dwordx4 v[42:45], v[10:11], off offset:384
	v_lshlrev_b64 v[16:17], 2, v[18:19]
	v_lshl_add_u64 v[46:47], s[4:5], 0, v[16:17]
	v_lshl_add_u64 v[16:17], s[10:11], 0, v[16:17]
	v_or_b32_e32 v18, 0x610, v14
	global_load_dword v95, v[16:17], off
	v_lshlrev_b64 v[16:17], 2, v[18:19]
	global_load_dword v94, v[46:47], off
	v_lshl_add_u64 v[46:47], s[4:5], 0, v[16:17]
	v_lshl_add_u64 v[16:17], s[10:11], 0, v[16:17]
	v_or_b32_e32 v18, 0x620, v14
	global_load_dword v97, v[16:17], off
	v_lshlrev_b64 v[16:17], 2, v[18:19]
	global_load_dword v96, v[46:47], off
	v_lshl_add_u64 v[46:47], s[4:5], 0, v[16:17]
	v_lshl_add_u64 v[16:17], s[10:11], 0, v[16:17]
	v_or_b32_e32 v18, 0x630, v14
	global_load_dword v99, v[16:17], off
	v_lshlrev_b64 v[16:17], 2, v[18:19]
	global_load_dword v98, v[46:47], off
	v_lshl_add_u64 v[46:47], s[4:5], 0, v[16:17]
	v_lshl_add_u64 v[16:17], s[10:11], 0, v[16:17]
	v_or_b32_e32 v18, 0x640, v14
	global_load_dword v101, v[16:17], off
	v_lshlrev_b64 v[16:17], 2, v[18:19]
	global_load_dword v100, v[46:47], off
	v_lshl_add_u64 v[46:47], s[4:5], 0, v[16:17]
	v_lshl_add_u64 v[16:17], s[10:11], 0, v[16:17]
	v_or_b32_e32 v18, 0x650, v14
	global_load_dword v103, v[16:17], off
	v_lshlrev_b64 v[16:17], 2, v[18:19]
	global_load_dword v102, v[46:47], off
	v_lshl_add_u64 v[46:47], s[4:5], 0, v[16:17]
	v_lshl_add_u64 v[16:17], s[10:11], 0, v[16:17]
	v_or_b32_e32 v18, 0x660, v14
	global_load_dword v105, v[16:17], off
	v_lshlrev_b64 v[16:17], 2, v[18:19]
	global_load_dword v104, v[46:47], off
	v_lshl_add_u64 v[46:47], s[4:5], 0, v[16:17]
	v_lshl_add_u64 v[16:17], s[10:11], 0, v[16:17]
	v_or_b32_e32 v18, 0x670, v14
	global_load_dword v107, v[16:17], off
	v_lshlrev_b64 v[16:17], 2, v[18:19]
	global_load_dword v106, v[46:47], off
	v_lshl_add_u64 v[46:47], s[4:5], 0, v[16:17]
	v_lshl_add_u64 v[16:17], s[10:11], 0, v[16:17]
	global_load_dword v18, v[46:47], off
	s_mov_b32 s23, 0
	global_load_dword v16, v[16:17], off
	s_load_dwordx2 s[24:25], s[0:1], 0x88
	s_load_dwordx4 s[12:15], s[0:1], 0x78
	s_load_dwordx4 s[16:19], s[0:1], 0x50
	s_waitcnt vmcnt(62)
	v_cvt_pk_f16_f32 v6, v6, v7
	v_cvt_pk_f16_f32 v7, v8, v9
	v_cvt_pk_f16_f32 v8, v2, v3
	v_cvt_pk_f16_f32 v9, v4, v5
	v_cvt_pk_f16_f32 v2, v37, v49
	v_cvt_pk_f16_f32 v3, v51, v53
	s_waitcnt vmcnt(59)
	v_cvt_pk_f16_f32 v4, v55, v57
	s_waitcnt vmcnt(55)
	v_cvt_pk_f16_f32 v5, v59, v61
	v_cvt_pk_f16_f32 v46, v48, v50
	v_cvt_pk_f16_f32 v47, v52, v54
	v_mfma_f32_16x16x32_f16 a[0:3], v[6:9], v[2:5], 0
	global_store_dwordx4 v108, v[6:9], s[26:27] offset:0
	v_cvt_pk_f16_f32 v48, v56, v58
	s_waitcnt vmcnt(55)
	v_cvt_pk_f16_f32 v49, v60, v62
	s_waitcnt vmcnt(53)
	v_cvt_pk_f16_f32 v2, v24, v25
	v_cvt_pk_f16_f32 v3, v26, v27
	v_cvt_pk_f16_f32 v4, v20, v21
	v_cvt_pk_f16_f32 v5, v22, v23
	v_mfma_f32_16x16x32_f16 a[4:7], v[6:9], v[46:49], 0
	s_waitcnt vmcnt(50)
	v_cvt_pk_f16_f32 v6, v63, v65
	s_waitcnt vmcnt(49)
	v_cvt_pk_f16_f32 v20, v64, v66
	s_waitcnt vmcnt(46)
	v_cvt_pk_f16_f32 v7, v67, v69
	s_waitcnt vmcnt(42)
	v_cvt_pk_f16_f32 v8, v71, v73
	s_waitcnt vmcnt(38)
	v_cvt_pk_f16_f32 v9, v75, v77
	v_cvt_pk_f16_f32 v21, v68, v70
	v_cvt_pk_f16_f32 v22, v72, v74
	s_waitcnt vmcnt(37)
	v_cvt_pk_f16_f32 v23, v76, v78
	v_mfma_f32_16x16x32_f16 a[0:3], v[2:5], v[6:9], a[0:3]
	global_store_dwordx4 v108, v[2:5], s[26:27] offset:64
	s_waitcnt vmcnt(32)
	v_cvt_pk_f16_f32 v6, v15, v80
	s_waitcnt vmcnt(28)
	v_cvt_pk_f16_f32 v7, v82, v84
	s_waitcnt vmcnt(24)
	v_cvt_pk_f16_f32 v8, v86, v88
	v_mfma_f32_16x16x32_f16 a[4:7], v[2:5], v[20:23], a[4:7]
	v_cvt_pk_f16_f32 v2, v32, v33
	v_cvt_pk_f16_f32 v3, v34, v35
	v_cvt_pk_f16_f32 v4, v28, v29
	v_cvt_pk_f16_f32 v5, v30, v31
	v_cvt_pk_f16_f32 v20, v79, v81
	s_waitcnt vmcnt(21)
	v_cvt_pk_f16_f32 v9, v90, v92
	v_cvt_pk_f16_f32 v21, v83, v85
	v_cvt_pk_f16_f32 v22, v87, v89
	s_waitcnt vmcnt(20)
	v_cvt_pk_f16_f32 v23, v91, v93
	v_mfma_f32_16x16x32_f16 a[0:3], v[2:5], v[6:9], a[0:3]
	global_store_dwordx4 v108, v[2:5], s[26:27] offset:128
	s_waitcnt vmcnt(15)
	v_cvt_pk_f16_f32 v6, v94, v96
	s_waitcnt vmcnt(11)
	v_cvt_pk_f16_f32 v7, v98, v100
	s_waitcnt vmcnt(7)
	v_cvt_pk_f16_f32 v8, v102, v104
	v_mfma_f32_16x16x32_f16 a[8:11], v[2:5], v[20:23], a[4:7]
	v_cvt_pk_f16_f32 v2, v42, v43
	v_cvt_pk_f16_f32 v3, v44, v45
	v_cvt_pk_f16_f32 v4, v38, v39
	v_cvt_pk_f16_f32 v5, v40, v41
	v_cvt_pk_f16_f32 v20, v95, v97
	s_waitcnt vmcnt(4)
	v_cvt_pk_f16_f32 v9, v106, v18
	v_cvt_pk_f16_f32 v21, v99, v101
	v_cvt_pk_f16_f32 v22, v103, v105
	s_waitcnt vmcnt(3)
	v_cvt_pk_f16_f32 v23, v107, v16
	v_mfma_f32_16x16x32_f16 a[4:7], v[2:5], v[6:9], a[0:3]
	global_store_dwordx4 v108, v[2:5], s[26:27] offset:192
	s_nop 0
	v_mfma_f32_16x16x32_f16 a[0:3], v[2:5], v[20:23], a[8:11]
	v_or_b32_e32 v18, 0x800, v14
	v_lshlrev_b64 v[16:17], 2, v[18:19]
	v_lshl_add_u64 v[20:21], s[4:5], 0, v[16:17]
	v_lshl_add_u64 v[16:17], s[10:11], 0, v[16:17]
	v_or_b32_e32 v18, 0x810, v14
	global_load_dwordx4 v[2:5], v[10:11], off offset:528
	global_load_dwordx4 v[6:9], v[10:11], off offset:512
	global_load_dword v46, v[16:17], off
	v_lshlrev_b64 v[16:17], 2, v[18:19]
	global_load_dword v37, v[20:21], off
	v_lshl_add_u64 v[20:21], s[4:5], 0, v[16:17]
	v_lshl_add_u64 v[16:17], s[10:11], 0, v[16:17]
	v_or_b32_e32 v18, 0x820, v14
	global_load_dword v48, v[16:17], off
	v_lshlrev_b64 v[16:17], 2, v[18:19]
	global_load_dword v47, v[20:21], off
	v_lshl_add_u64 v[20:21], s[4:5], 0, v[16:17]
	v_lshl_add_u64 v[16:17], s[10:11], 0, v[16:17]
	v_or_b32_e32 v18, 0x830, v14
	global_load_dword v50, v[16:17], off
	v_lshlrev_b64 v[16:17], 2, v[18:19]
	global_load_dword v49, v[20:21], off
	v_lshl_add_u64 v[20:21], s[4:5], 0, v[16:17]
	v_lshl_add_u64 v[16:17], s[10:11], 0, v[16:17]
	v_or_b32_e32 v18, 0x840, v14
	global_load_dword v52, v[16:17], off
	v_lshlrev_b64 v[16:17], 2, v[18:19]
	global_load_dword v51, v[20:21], off
	v_lshl_add_u64 v[20:21], s[4:5], 0, v[16:17]
	v_lshl_add_u64 v[16:17], s[10:11], 0, v[16:17]
	v_or_b32_e32 v18, 0x850, v14
	global_load_dword v54, v[16:17], off
	v_lshlrev_b64 v[16:17], 2, v[18:19]
	global_load_dword v53, v[20:21], off
	v_lshl_add_u64 v[20:21], s[4:5], 0, v[16:17]
	v_lshl_add_u64 v[16:17], s[10:11], 0, v[16:17]
	v_or_b32_e32 v18, 0x860, v14
	global_load_dword v56, v[16:17], off
	v_lshlrev_b64 v[16:17], 2, v[18:19]
	global_load_dword v55, v[20:21], off
	v_lshl_add_u64 v[20:21], s[4:5], 0, v[16:17]
	v_lshl_add_u64 v[16:17], s[10:11], 0, v[16:17]
	v_or_b32_e32 v18, 0x870, v14
	global_load_dword v58, v[16:17], off
	v_lshlrev_b64 v[16:17], 2, v[18:19]
	global_load_dword v57, v[20:21], off
	v_lshl_add_u64 v[20:21], s[4:5], 0, v[16:17]
	v_lshl_add_u64 v[16:17], s[10:11], 0, v[16:17]
	v_or_b32_e32 v18, 0xa00, v14
	global_load_dword v59, v[20:21], off
	global_load_dword v60, v[16:17], off
	s_nop 0
	global_load_dwordx4 v[20:23], v[10:11], off offset:656
	global_load_dwordx4 v[24:27], v[10:11], off offset:640
	v_lshlrev_b64 v[16:17], 2, v[18:19]
	v_lshl_add_u64 v[28:29], s[4:5], 0, v[16:17]
	v_lshl_add_u64 v[16:17], s[10:11], 0, v[16:17]
	v_or_b32_e32 v18, 0xa10, v14
	global_load_dword v62, v[16:17], off
	v_lshlrev_b64 v[16:17], 2, v[18:19]
	global_load_dword v61, v[28:29], off
	v_lshl_add_u64 v[28:29], s[4:5], 0, v[16:17]
	v_lshl_add_u64 v[16:17], s[10:11], 0, v[16:17]
	v_or_b32_e32 v18, 0xa20, v14
	global_load_dword v64, v[16:17], off
	v_lshlrev_b64 v[16:17], 2, v[18:19]
	global_load_dword v63, v[28:29], off
	v_lshl_add_u64 v[28:29], s[4:5], 0, v[16:17]
	v_lshl_add_u64 v[16:17], s[10:11], 0, v[16:17]
	v_or_b32_e32 v18, 0xa30, v14
	global_load_dword v66, v[16:17], off
	v_lshlrev_b64 v[16:17], 2, v[18:19]
	global_load_dword v65, v[28:29], off
	v_lshl_add_u64 v[28:29], s[4:5], 0, v[16:17]
	v_lshl_add_u64 v[16:17], s[10:11], 0, v[16:17]
	v_or_b32_e32 v18, 0xa40, v14
	global_load_dword v68, v[16:17], off
	v_lshlrev_b64 v[16:17], 2, v[18:19]
	global_load_dword v67, v[28:29], off
	v_lshl_add_u64 v[28:29], s[4:5], 0, v[16:17]
	v_lshl_add_u64 v[16:17], s[10:11], 0, v[16:17]
	v_or_b32_e32 v18, 0xa50, v14
	global_load_dword v70, v[16:17], off
	v_lshlrev_b64 v[16:17], 2, v[18:19]
	global_load_dword v69, v[28:29], off
	v_lshl_add_u64 v[28:29], s[4:5], 0, v[16:17]
	v_lshl_add_u64 v[16:17], s[10:11], 0, v[16:17]
	v_or_b32_e32 v18, 0xa60, v14
	global_load_dword v72, v[16:17], off
	v_lshlrev_b64 v[16:17], 2, v[18:19]
	global_load_dword v71, v[28:29], off
	v_lshl_add_u64 v[28:29], s[4:5], 0, v[16:17]
	v_lshl_add_u64 v[16:17], s[10:11], 0, v[16:17]
	v_or_b32_e32 v18, 0xa70, v14
	global_load_dword v74, v[16:17], off
	v_lshlrev_b64 v[16:17], 2, v[18:19]
	global_load_dword v73, v[28:29], off
	v_lshl_add_u64 v[28:29], s[4:5], 0, v[16:17]
	v_lshl_add_u64 v[16:17], s[10:11], 0, v[16:17]
	v_or_b32_e32 v18, 0xc00, v14
	global_load_dword v75, v[28:29], off
	global_load_dword v76, v[16:17], off
	s_nop 0
	global_load_dwordx4 v[28:31], v[10:11], off offset:784
	global_load_dwordx4 v[32:35], v[10:11], off offset:768
	v_lshlrev_b64 v[16:17], 2, v[18:19]
	v_lshl_add_u64 v[38:39], s[4:5], 0, v[16:17]
	v_lshl_add_u64 v[16:17], s[10:11], 0, v[16:17]
	v_or_b32_e32 v18, 0xc10, v14
	global_load_dword v78, v[16:17], off
	v_lshlrev_b64 v[16:17], 2, v[18:19]
	global_load_dword v77, v[38:39], off
	v_lshl_add_u64 v[38:39], s[4:5], 0, v[16:17]
	v_lshl_add_u64 v[16:17], s[10:11], 0, v[16:17]
	v_or_b32_e32 v18, 0xc20, v14
	global_load_dword v80, v[16:17], off
	v_lshlrev_b64 v[16:17], 2, v[18:19]
	global_load_dword v79, v[38:39], off
	v_lshl_add_u64 v[38:39], s[4:5], 0, v[16:17]
	v_lshl_add_u64 v[16:17], s[10:11], 0, v[16:17]
	v_or_b32_e32 v18, 0xc30, v14
	global_load_dword v82, v[16:17], off
	v_lshlrev_b64 v[16:17], 2, v[18:19]
	global_load_dword v81, v[38:39], off
	v_lshl_add_u64 v[38:39], s[4:5], 0, v[16:17]
	v_lshl_add_u64 v[16:17], s[10:11], 0, v[16:17]
	v_or_b32_e32 v18, 0xc40, v14
	global_load_dword v84, v[16:17], off
	v_lshlrev_b64 v[16:17], 2, v[18:19]
	global_load_dword v83, v[38:39], off
	v_lshl_add_u64 v[38:39], s[4:5], 0, v[16:17]
	v_lshl_add_u64 v[16:17], s[10:11], 0, v[16:17]
	v_or_b32_e32 v18, 0xc50, v14
	global_load_dword v86, v[16:17], off
	v_lshlrev_b64 v[16:17], 2, v[18:19]
	global_load_dword v85, v[38:39], off
	v_lshl_add_u64 v[38:39], s[4:5], 0, v[16:17]
	v_lshl_add_u64 v[16:17], s[10:11], 0, v[16:17]
	v_or_b32_e32 v18, 0xc60, v14
	global_load_dword v88, v[16:17], off
	v_lshlrev_b64 v[16:17], 2, v[18:19]
	global_load_dword v87, v[38:39], off
	v_lshl_add_u64 v[38:39], s[4:5], 0, v[16:17]
	v_lshl_add_u64 v[16:17], s[10:11], 0, v[16:17]
	v_or_b32_e32 v18, 0xc70, v14
	global_load_dword v90, v[16:17], off
	v_lshlrev_b64 v[16:17], 2, v[18:19]
	global_load_dword v89, v[38:39], off
	v_lshl_add_u64 v[38:39], s[4:5], 0, v[16:17]
	v_lshl_add_u64 v[16:17], s[10:11], 0, v[16:17]
	v_or_b32_e32 v18, 0xe00, v14
	global_load_dword v91, v[38:39], off
	global_load_dword v92, v[16:17], off
	s_nop 0
	global_load_dwordx4 v[38:41], v[10:11], off offset:912
	global_load_dwordx4 v[42:45], v[10:11], off offset:896
	v_lshlrev_b64 v[10:11], 2, v[18:19]
	v_lshl_add_u64 v[16:17], s[4:5], 0, v[10:11]
	v_lshl_add_u64 v[10:11], s[10:11], 0, v[10:11]
	v_or_b32_e32 v18, 0xe10, v14
	global_load_dword v94, v[10:11], off
	v_lshlrev_b64 v[10:11], 2, v[18:19]
	global_load_dword v93, v[16:17], off
	v_lshl_add_u64 v[16:17], s[4:5], 0, v[10:11]
	v_lshl_add_u64 v[10:11], s[10:11], 0, v[10:11]
	v_or_b32_e32 v18, 0xe20, v14
	global_load_dword v96, v[10:11], off
	v_lshlrev_b64 v[10:11], 2, v[18:19]
	global_load_dword v95, v[16:17], off
	v_lshl_add_u64 v[16:17], s[4:5], 0, v[10:11]
	v_lshl_add_u64 v[10:11], s[10:11], 0, v[10:11]
	v_or_b32_e32 v18, 0xe30, v14
	global_load_dword v98, v[10:11], off
	v_lshlrev_b64 v[10:11], 2, v[18:19]
	global_load_dword v97, v[16:17], off
	v_lshl_add_u64 v[16:17], s[4:5], 0, v[10:11]
	v_lshl_add_u64 v[10:11], s[10:11], 0, v[10:11]
	v_or_b32_e32 v18, 0xe40, v14
	global_load_dword v100, v[10:11], off
	v_lshlrev_b64 v[10:11], 2, v[18:19]
	global_load_dword v99, v[16:17], off
	v_lshl_add_u64 v[16:17], s[4:5], 0, v[10:11]
	v_lshl_add_u64 v[10:11], s[10:11], 0, v[10:11]
	v_or_b32_e32 v18, 0xe50, v14
	global_load_dword v102, v[10:11], off
	v_lshlrev_b64 v[10:11], 2, v[18:19]
	global_load_dword v101, v[16:17], off
	v_lshl_add_u64 v[16:17], s[4:5], 0, v[10:11]
	v_lshl_add_u64 v[10:11], s[10:11], 0, v[10:11]
	v_or_b32_e32 v18, 0xe60, v14
	global_load_dword v104, v[10:11], off
	v_lshlrev_b64 v[10:11], 2, v[18:19]
	global_load_dword v103, v[16:17], off
	v_lshl_add_u64 v[16:17], s[4:5], 0, v[10:11]
	v_lshl_add_u64 v[10:11], s[10:11], 0, v[10:11]
	v_or_b32_e32 v18, 0xe70, v14
	global_load_dword v106, v[10:11], off
	v_lshlrev_b64 v[10:11], 2, v[18:19]
	v_lshl_add_u64 v[14:15], s[4:5], 0, v[10:11]
	v_lshl_add_u64 v[10:11], s[10:11], 0, v[10:11]
	global_load_dword v105, v[16:17], off
	global_load_dword v18, v[14:15], off
	s_nop 0
	global_load_dword v10, v[10:11], off
	s_waitcnt vmcnt(62)
	v_cvt_pk_f16_f32 v6, v6, v7
	v_cvt_pk_f16_f32 v7, v8, v9
	v_cvt_pk_f16_f32 v8, v2, v3
	v_cvt_pk_f16_f32 v9, v4, v5
	v_cvt_pk_f16_f32 v2, v37, v47
	v_cvt_pk_f16_f32 v3, v49, v51
	s_waitcnt vmcnt(58)
	v_cvt_pk_f16_f32 v4, v53, v55
	s_waitcnt vmcnt(55)
	v_cvt_pk_f16_f32 v5, v57, v59
	s_waitcnt vmcnt(49)
	v_cvt_pk_f16_f32 v14, v62, v64
	s_waitcnt vmcnt(45)
	v_cvt_pk_f16_f32 v15, v66, v68
	v_mfma_f32_16x16x32_f16 a[4:7], v[6:9], v[2:5], a[4:7]
	global_store_dwordx4 v108, v[6:9], s[26:27] offset:256
	v_cvt_pk_f16_f32 v2, v46, v48
	v_cvt_pk_f16_f32 v3, v50, v52
	v_cvt_pk_f16_f32 v4, v54, v56
	v_cvt_pk_f16_f32 v5, v58, v60
	s_waitcnt vmcnt(42)
	v_cvt_pk_f16_f32 v16, v70, v72
	s_waitcnt vmcnt(37)
	v_cvt_pk_f16_f32 v17, v74, v76
	v_mfma_f32_16x16x32_f16 a[0:3], v[6:9], v[2:5], a[0:3]
	v_cvt_pk_f16_f32 v2, v24, v25
	v_cvt_pk_f16_f32 v3, v26, v27
	v_cvt_pk_f16_f32 v4, v20, v21
	v_cvt_pk_f16_f32 v5, v22, v23
	v_cvt_pk_f16_f32 v6, v61, v63
	v_cvt_pk_f16_f32 v7, v65, v67
	v_cvt_pk_f16_f32 v8, v69, v71
	v_cvt_pk_f16_f32 v9, v73, v75
	v_mfma_f32_16x16x32_f16 a[0:3], v[2:5], v[14:17], a[0:3]
	global_store_dwordx4 v108, v[2:5], s[26:27] offset:320
	s_waitcnt vmcnt(33)
	v_cvt_pk_f16_f32 v14, v78, v80
	s_waitcnt vmcnt(29)
	v_cvt_pk_f16_f32 v15, v82, v84
	s_waitcnt vmcnt(25)
	v_cvt_pk_f16_f32 v16, v86, v88
	v_mfma_f32_16x16x32_f16 a[4:7], v[2:5], v[6:9], a[4:7]
	v_cvt_pk_f16_f32 v2, v32, v33
	v_cvt_pk_f16_f32 v3, v34, v35
	v_cvt_pk_f16_f32 v4, v28, v29
	v_cvt_pk_f16_f32 v5, v30, v31
	v_cvt_pk_f16_f32 v6, v77, v79
	v_cvt_pk_f16_f32 v7, v81, v83
	s_waitcnt vmcnt(24)
	v_cvt_pk_f16_f32 v8, v85, v87
	s_waitcnt vmcnt(21)
	v_cvt_pk_f16_f32 v9, v89, v91
	s_waitcnt vmcnt(20)
	v_cvt_pk_f16_f32 v17, v90, v92
	v_mfma_f32_16x16x32_f16 a[4:7], v[2:5], v[6:9], a[4:7]
	global_store_dwordx4 v108, v[2:5], s[26:27] offset:384
	s_waitcnt vmcnt(15)
	v_cvt_pk_f16_f32 v6, v93, v95
	s_waitcnt vmcnt(11)
	v_cvt_pk_f16_f32 v7, v97, v99
	s_waitcnt vmcnt(7)
	v_cvt_pk_f16_f32 v8, v101, v103
	v_mfma_f32_16x16x32_f16 a[0:3], v[2:5], v[14:17], a[0:3]
	v_cvt_pk_f16_f32 v2, v42, v43
	v_cvt_pk_f16_f32 v3, v44, v45
	v_cvt_pk_f16_f32 v4, v38, v39
	v_cvt_pk_f16_f32 v5, v40, v41
	v_cvt_pk_f16_f32 v14, v94, v96
	s_waitcnt vmcnt(4)
	v_cvt_pk_f16_f32 v9, v105, v18
	v_cvt_pk_f16_f32 v15, v98, v100
	v_cvt_pk_f16_f32 v16, v102, v104
	s_waitcnt vmcnt(3)
	v_cvt_pk_f16_f32 v17, v106, v10
	v_mfma_f32_16x16x32_f16 a[4:7], v[2:5], v[6:9], a[4:7]
	global_store_dwordx4 v108, v[2:5], s[26:27] offset:448
	s_nop 0
	v_mfma_f32_16x16x32_f16 a[0:3], v[2:5], v[14:17], a[0:3]
	v_lshlrev_b32_e32 v2, 11, v1
	v_lshlrev_b32_e32 v3, 2, v12
	v_lshlrev_b32_e32 v4, 8, v13
	v_lshlrev_b32_e32 v18, 2, v0
	s_movk_i32 s4, 0x3c0
	v_or3_b32 v2, v2, v3, v4
	v_and_or_b32 v10, v18, s4, v3
	ds_write_b32 v2, a4
	ds_write_b32 v2, a0 offset:1024
	ds_write_b32 v2, a5 offset:64
	ds_write_b32 v2, a1 offset:1088
	ds_write_b32 v2, a6 offset:128
	ds_write_b32 v2, a2 offset:1152
	ds_write_b32 v2, a7 offset:192
	ds_write_b32 v2, a3 offset:1216
	s_waitcnt lgkmcnt(0)
	s_barrier
	ds_read2st64_b32 v[2:3], v10 offset1:4
	ds_read2st64_b32 v[4:5], v10 offset0:8 offset1:12
	ds_read2st64_b32 v[6:7], v10 offset0:16 offset1:20
	ds_read2st64_b32 v[8:9], v10 offset0:24 offset1:28
	s_movk_i32 s4, 0x1000
	v_or_b32_e32 v20, 0x2000, v18
	s_waitcnt lgkmcnt(2)
	v_add_f32_e32 v2, v2, v4
	v_add_f32_e32 v3, v3, v5
	s_waitcnt lgkmcnt(1)
	v_add_f32_e32 v2, v2, v6
	v_add_f32_e32 v3, v3, v7
	v_lshl_add_u64 v[6:7], s[6:7], 0, v[18:19]
	s_waitcnt lgkmcnt(0)
	v_add_f32_e32 v2, v2, v8
	v_add_f32_e32 v3, v3, v9
	v_add_co_u32_e32 v4, vcc, s4, v6
	ds_write2st64_b32 v10, v2, v3 offset0:32 offset1:36
	v_or_b32_e32 v10, 0x1000, v18
	v_addc_co_u32_e32 v5, vcc, 0, v7, vcc
	s_waitcnt lgkmcnt(0)
	s_barrier
	global_load_dword v2, v18, s[6:7] offset:2048
	global_load_dword v3, v18, s[6:7] offset:3072
	global_load_dword v57, v10, s[6:7]
	global_load_dword v49, v[4:5], off offset:1024
	global_load_dword v50, v[4:5], off offset:2048
	global_load_dword v44, v[4:5], off offset:3072
	global_load_dword v51, v10, s[16:17]
	global_load_dword v13, v18, s[6:7]
	s_nop 0
	global_load_dword v5, v18, s[16:17]
	global_load_dword v10, v18, s[6:7] offset:1024
	global_load_dword v11, v18, s[16:17] offset:1024
	global_load_dword v4, v18, s[16:17] offset:2048
	global_load_dword v42, v18, s[8:9]
	global_load_dword v12, v18, s[16:17] offset:3072
	global_load_dword v40, v18, s[18:19]
	v_lshl_add_u64 v[8:9], s[16:17], 0, v[18:19]
	v_add_co_u32_e32 v14, vcc, s4, v8
	s_movk_i32 s4, 0x2000
	s_nop 0
	v_addc_co_u32_e32 v15, vcc, 0, v9, vcc
	v_add_co_u32_e32 v16, vcc, s4, v6
	s_mov_b32 s5, 0xc2000000
	s_nop 0
	v_addc_co_u32_e32 v17, vcc, 0, v7, vcc
	global_load_dword v56, v[14:15], off offset:1024
	global_load_dword v54, v[14:15], off offset:2048
	global_load_dword v52, v[14:15], off offset:3072
	global_load_dword v53, v20, s[6:7]
	global_load_dword v43, v[16:17], off offset:1024
	global_load_dword v30, v[16:17], off offset:2048
	global_load_dword v31, v[16:17], off offset:3072
	global_load_dword v45, v20, s[16:17]
	v_add_co_u32_e32 v14, vcc, s4, v8
	s_movk_i32 s4, 0x3000
	s_nop 0
	v_addc_co_u32_e32 v15, vcc, 0, v9, vcc
	v_add_co_u32_e32 v6, vcc, s4, v6
	v_or_b32_e32 v16, 0x3000, v18
	s_nop 0
	v_addc_co_u32_e32 v7, vcc, 0, v7, vcc
	global_load_dword v46, v[14:15], off offset:1024
	global_load_dword v34, v[14:15], off offset:2048
	global_load_dword v35, v[14:15], off offset:3072
	global_load_dword v32, v16, s[6:7]
	global_load_dword v33, v[6:7], off offset:1024
	global_load_dword v20, v[6:7], off offset:2048
	global_load_dword v21, v[6:7], off offset:3072
	global_load_dword v22, v16, s[16:17]
	v_add_co_u32_e32 v6, vcc, s4, v8
	s_and_b32 s4, s2, 0xffffff80
	s_nop 0
	v_addc_co_u32_e32 v7, vcc, 0, v9, vcc
	global_load_dword v23, v[6:7], off offset:1024
	global_load_dword v24, v[6:7], off offset:2048
	global_load_dword v25, v[6:7], off offset:3072
	v_lshl_or_b32 v6, v1, 5, s4
	s_lshr_b32 s4, s2, 2
	v_and_or_b32 v70, s4, 31, v6
	ds_read_b128 v[6:9], v19 offset:8192
	ds_read_b128 v[14:17], v19 offset:9216
	ds_read_b128 v[26:29], v19 offset:8208
	ds_read_b128 v[58:61], v19 offset:8224
	ds_read_b128 v[62:65], v19 offset:8240
	v_lshlrev_b32_e32 v18, 1, v36
	ds_read_b128 v[66:69], v19 offset:9232
	v_lshl_add_u64 v[72:73], s[24:25], 0, v[18:19]
	v_mov_b32_e32 v38, 0x42000000
	v_ashrrev_i32_e32 v71, 31, v70
	s_and_b32 s4, s22, 48
	s_lshl_b32 s22, s4, 7
	s_lshl_b32 s4, s4, 1
	s_waitcnt vmcnt(21) lgkmcnt(5)
	v_fma_f32 v18, v13, v6, v42
	v_fmac_f32_e32 v18, v10, v7
	s_waitcnt vmcnt(19) lgkmcnt(4)
	v_fma_f32 v37, v5, v14, v40
	v_fmac_f32_e32 v37, v11, v15
	v_fmac_f32_e32 v18, v2, v8
	v_fmac_f32_e32 v37, v4, v16
	v_fmac_f32_e32 v18, v3, v9
	v_fmac_f32_e32 v37, v12, v17
	ds_read_b128 v[6:9], v19 offset:9248
	s_waitcnt lgkmcnt(4)
	v_fmac_f32_e32 v18, v57, v26
	s_waitcnt lgkmcnt(1)
	v_fmac_f32_e32 v37, v51, v66
	v_fmac_f32_e32 v18, v49, v27
	s_waitcnt vmcnt(18)
	v_fmac_f32_e32 v37, v56, v67
	v_fmac_f32_e32 v18, v50, v28
	s_waitcnt vmcnt(17)
	v_fmac_f32_e32 v37, v54, v68
	v_fmac_f32_e32 v18, v44, v29
	s_waitcnt vmcnt(16)
	v_fmac_f32_e32 v37, v52, v69
	s_waitcnt vmcnt(15)
	v_fmac_f32_e32 v18, v53, v58
	s_waitcnt vmcnt(11) lgkmcnt(0)
	v_fmac_f32_e32 v37, v45, v6
	v_fmac_f32_e32 v18, v43, v59
	s_waitcnt vmcnt(10)
	v_fmac_f32_e32 v37, v46, v7
	v_pk_mul_f32 v[6:7], v[30:31], v[60:61]
	ds_read_b128 v[14:17], v19 offset:9264
	v_add_f32_e32 v6, v18, v6
	v_add_f32_e32 v18, v6, v7
	s_waitcnt vmcnt(8)
	v_pk_mul_f32 v[6:7], v[34:35], v[8:9]
	v_lshlrev_b64 v[26:27], 13, v[70:71]
	v_add_f32_e32 v6, v37, v6
	v_add_f32_e32 v8, v6, v7
	s_waitcnt vmcnt(6)
	v_pk_mul_f32 v[6:7], v[32:33], v[62:63]
	s_nop 0
	v_add_f32_e32 v6, v18, v6
	v_add_f32_e32 v9, v6, v7
	s_waitcnt vmcnt(2) lgkmcnt(0)
	v_pk_mul_f32 v[6:7], v[22:23], v[14:15]
	s_nop 0
	v_add_f32_e32 v6, v8, v6
	v_add_f32_e32 v8, v6, v7
	v_pk_mul_f32 v[6:7], v[20:21], v[64:65]
	s_nop 0
	v_add_f32_e32 v6, v9, v6
	v_add_f32_e32 v9, v6, v7
	s_waitcnt vmcnt(0)
	v_pk_mul_f32 v[6:7], v[24:25], v[16:17]
	s_nop 0
	v_add_f32_e32 v6, v8, v6
	v_add_f32_e32 v6, v6, v7
	v_med3_f32 v6, v6, s5, v38
	v_mul_f32_e32 v6, 0x3fb8aa3b, v6
	v_exp_f32_e32 v18, v6
	v_med3_f32 v6, v9, s5, v38
	v_mul_f32_e32 v6, 0x3fb8aa3b, v6
	v_exp_f32_e32 v37, v6
	v_lshl_add_u64 v[6:7], v[72:73], 0, v[26:27]
	v_cvt_pk_bf16_f32 v8, v18, s0
	v_lshl_add_u64 v[28:29], v[6:7], 0, s[22:23]
	global_store_short v[28:29], v8, off
	ds_read_b128 v[6:9], v19 offset:8256
	ds_read_b128 v[14:17], v19 offset:9280
	ds_read_b128 v[58:61], v19 offset:8272
	ds_read_b128 v[62:65], v19 offset:8288
	ds_read_b128 v[66:69], v19 offset:8304
	ds_read_b128 v[70:73], v19 offset:9296
	s_waitcnt lgkmcnt(5)
	v_fma_f32 v39, v13, v6, v42
	s_waitcnt lgkmcnt(4)
	v_fma_f32 v41, v5, v14, v40
	v_fmac_f32_e32 v39, v10, v7
	v_fmac_f32_e32 v41, v11, v15
	v_fmac_f32_e32 v39, v2, v8
	v_fmac_f32_e32 v41, v4, v16
	v_fmac_f32_e32 v39, v3, v9
	v_fmac_f32_e32 v41, v12, v17
	ds_read_b128 v[6:9], v19 offset:9312
	s_waitcnt lgkmcnt(4)
	v_fmac_f32_e32 v39, v57, v58
	s_waitcnt lgkmcnt(1)
	v_fmac_f32_e32 v41, v51, v70
	v_fmac_f32_e32 v39, v49, v59
	v_fmac_f32_e32 v41, v56, v71
	v_fmac_f32_e32 v39, v50, v60
	v_fmac_f32_e32 v41, v54, v72
	v_fmac_f32_e32 v39, v44, v61
	v_fmac_f32_e32 v41, v52, v73
	v_fmac_f32_e32 v39, v53, v62
	s_waitcnt lgkmcnt(0)
	v_fmac_f32_e32 v41, v45, v6
	v_fmac_f32_e32 v39, v43, v63
	v_fmac_f32_e32 v41, v46, v7
	v_pk_mul_f32 v[6:7], v[30:31], v[64:65]
	ds_read_b128 v[14:17], v19 offset:9328
	v_add_f32_e32 v6, v39, v6
	v_add_f32_e32 v39, v6, v7
	v_pk_mul_f32 v[6:7], v[34:35], v[8:9]
	s_nop 0
	v_add_f32_e32 v6, v41, v6
	v_add_f32_e32 v8, v6, v7
	v_pk_mul_f32 v[6:7], v[32:33], v[66:67]
	s_nop 0
	v_add_f32_e32 v6, v39, v6
	v_add_f32_e32 v9, v6, v7
	s_waitcnt lgkmcnt(0)
	v_pk_mul_f32 v[6:7], v[22:23], v[14:15]
	s_nop 0
	v_add_f32_e32 v6, v8, v6
	v_add_f32_e32 v8, v6, v7
	v_pk_mul_f32 v[6:7], v[20:21], v[68:69]
	s_nop 0
	v_add_f32_e32 v6, v9, v6
	v_add_f32_e32 v9, v6, v7
	v_pk_mul_f32 v[6:7], v[24:25], v[16:17]
	s_nop 0
	v_add_f32_e32 v6, v8, v6
	v_add_f32_e32 v6, v6, v7
	v_med3_f32 v6, v6, s5, v38
	v_mul_f32_e32 v6, 0x3fb8aa3b, v6
	v_med3_f32 v7, v9, s5, v38
	v_exp_f32_e32 v39, v6
	v_mul_f32_e32 v41, 0x3fb8aa3b, v7
	ds_read_b128 v[6:9], v19 offset:8320
	ds_read_b128 v[14:17], v19 offset:9344
	ds_read_b128 v[58:61], v19 offset:8336
	ds_read_b128 v[62:65], v19 offset:9360
	v_cvt_pk_bf16_f32 v47, v39, s0
	global_store_short v[28:29], v47, off offset:128
	s_waitcnt lgkmcnt(3)
	v_fma_f32 v47, v13, v6, v42
	s_waitcnt lgkmcnt(2)
	v_fma_f32 v48, v5, v14, v40
	v_fmac_f32_e32 v47, v10, v7
	v_fmac_f32_e32 v48, v11, v15
	v_fmac_f32_e32 v47, v2, v8
	v_fmac_f32_e32 v48, v4, v16
	v_fmac_f32_e32 v47, v3, v9
	v_fmac_f32_e32 v48, v12, v17
	s_waitcnt lgkmcnt(1)
	v_fmac_f32_e32 v47, v57, v58
	ds_read_b128 v[6:9], v19 offset:8352
	ds_read_b128 v[14:17], v19 offset:9376
	v_fmac_f32_e32 v47, v49, v59
	s_waitcnt lgkmcnt(2)
	v_fmac_f32_e32 v48, v51, v62
	v_fmac_f32_e32 v47, v50, v60
	v_fmac_f32_e32 v48, v56, v63
	v_fmac_f32_e32 v47, v44, v61
	v_fmac_f32_e32 v48, v54, v64
	ds_read_b128 v[58:61], v19 offset:8368
	s_waitcnt lgkmcnt(2)
	v_fmac_f32_e32 v47, v53, v6
	v_fmac_f32_e32 v48, v52, v65
	v_fmac_f32_e32 v47, v43, v7
	v_pk_mul_f32 v[6:7], v[30:31], v[8:9]
	ds_read_b128 v[62:65], v19 offset:9392
	s_waitcnt lgkmcnt(2)
	v_fmac_f32_e32 v48, v45, v14
	v_add_f32_e32 v6, v47, v6
	v_fmac_f32_e32 v48, v46, v15
	v_add_f32_e32 v8, v6, v7
	v_pk_mul_f32 v[6:7], v[34:35], v[16:17]
	v_exp_f32_e32 v41, v41
	v_add_f32_e32 v6, v48, v6
	v_add_f32_e32 v9, v6, v7
	s_waitcnt lgkmcnt(1)
	v_pk_mul_f32 v[6:7], v[32:33], v[58:59]
	s_nop 0
	v_add_f32_e32 v6, v8, v6
	v_add_f32_e32 v8, v6, v7
	s_waitcnt lgkmcnt(0)
	v_pk_mul_f32 v[6:7], v[22:23], v[62:63]
	s_nop 0
	v_add_f32_e32 v6, v9, v6
	v_add_f32_e32 v9, v6, v7
	v_pk_mul_f32 v[6:7], v[20:21], v[60:61]
	s_nop 0
	v_add_f32_e32 v6, v8, v6
	v_add_f32_e32 v8, v6, v7
	v_pk_mul_f32 v[6:7], v[24:25], v[64:65]
	s_nop 0
	v_add_f32_e32 v6, v9, v6
	v_add_f32_e32 v6, v6, v7
	v_med3_f32 v6, v6, s5, v38
	v_mul_f32_e32 v6, 0x3fb8aa3b, v6
	v_exp_f32_e32 v47, v6
	v_med3_f32 v6, v8, s5, v38
	v_mul_f32_e32 v6, 0x3fb8aa3b, v6
	v_exp_f32_e32 v48, v6
	v_cvt_pk_bf16_f32 v6, v47, s0
	global_store_short v[28:29], v6, off offset:256
	ds_read_b128 v[6:9], v19 offset:8384
	ds_read_b128 v[14:17], v19 offset:9408
	ds_read_b128 v[58:61], v19 offset:8400
	ds_read_b128 v[62:65], v19 offset:8416
	ds_read_b128 v[66:69], v19 offset:8432
	ds_read_b128 v[70:73], v19 offset:9424
	s_waitcnt lgkmcnt(5)
	v_fma_f32 v55, v13, v6, v42
	s_waitcnt lgkmcnt(4)
	v_fma_f32 v74, v5, v14, v40
	v_fmac_f32_e32 v55, v10, v7
	v_fmac_f32_e32 v74, v11, v15
	v_fmac_f32_e32 v55, v2, v8
	v_fmac_f32_e32 v74, v4, v16
	v_fmac_f32_e32 v55, v3, v9
	v_fmac_f32_e32 v74, v12, v17
	ds_read_b128 v[6:9], v19 offset:9440
	s_waitcnt lgkmcnt(4)
	v_fmac_f32_e32 v55, v57, v58
	s_waitcnt lgkmcnt(1)
	v_fmac_f32_e32 v74, v51, v70
	v_fmac_f32_e32 v55, v49, v59
	v_fmac_f32_e32 v74, v56, v71
	v_fmac_f32_e32 v55, v50, v60
	v_fmac_f32_e32 v74, v54, v72
	v_fmac_f32_e32 v55, v44, v61
	v_fmac_f32_e32 v74, v52, v73
	v_fmac_f32_e32 v55, v53, v62
	s_waitcnt lgkmcnt(0)
	v_fmac_f32_e32 v74, v45, v6
	v_fmac_f32_e32 v55, v43, v63
	v_fmac_f32_e32 v74, v46, v7
	v_pk_mul_f32 v[6:7], v[30:31], v[64:65]
	ds_read_b128 v[14:17], v19 offset:9456
	v_add_f32_e32 v6, v55, v6
	v_add_f32_e32 v55, v6, v7
	v_pk_mul_f32 v[6:7], v[34:35], v[8:9]
	s_nop 0
	v_add_f32_e32 v6, v74, v6
	v_add_f32_e32 v8, v6, v7
	v_pk_mul_f32 v[6:7], v[32:33], v[66:67]
	s_nop 0
	v_add_f32_e32 v6, v55, v6
	v_add_f32_e32 v9, v6, v7
	s_waitcnt lgkmcnt(0)
	v_pk_mul_f32 v[6:7], v[22:23], v[14:15]
	s_nop 0
	v_add_f32_e32 v6, v8, v6
	v_add_f32_e32 v8, v6, v7
	v_pk_mul_f32 v[6:7], v[20:21], v[68:69]
	s_nop 0
	v_add_f32_e32 v6, v9, v6
	v_add_f32_e32 v9, v6, v7
	v_pk_mul_f32 v[6:7], v[24:25], v[16:17]
	s_nop 0
	v_add_f32_e32 v6, v8, v6
	v_add_f32_e32 v6, v6, v7
	v_med3_f32 v6, v6, s5, v38
	v_mul_f32_e32 v6, 0x3fb8aa3b, v6
	v_med3_f32 v7, v9, s5, v38
	v_exp_f32_e32 v55, v6
	v_mul_f32_e32 v58, 0x3fb8aa3b, v7
	ds_read_b128 v[6:9], v19 offset:8448
	ds_read_b128 v[14:17], v19 offset:9472
	ds_read_b128 v[60:63], v19 offset:8464
	ds_read_b128 v[64:67], v19 offset:9488
	v_cvt_pk_bf16_f32 v59, v55, s0
	global_store_short v[28:29], v59, off offset:384
	s_waitcnt lgkmcnt(3)
	v_fma_f32 v59, v13, v6, v42
	s_waitcnt lgkmcnt(2)
	v_fma_f32 v68, v5, v14, v40
	v_fmac_f32_e32 v59, v10, v7
	v_fmac_f32_e32 v68, v11, v15
	v_fmac_f32_e32 v59, v2, v8
	v_fmac_f32_e32 v68, v4, v16
	v_fmac_f32_e32 v59, v3, v9
	v_fmac_f32_e32 v68, v12, v17
	s_waitcnt lgkmcnt(1)
	v_fmac_f32_e32 v59, v57, v60
	ds_read_b128 v[6:9], v19 offset:8480
	ds_read_b128 v[14:17], v19 offset:9504
	v_fmac_f32_e32 v59, v49, v61
	s_waitcnt lgkmcnt(2)
	v_fmac_f32_e32 v68, v51, v64
	v_fmac_f32_e32 v59, v50, v62
	v_fmac_f32_e32 v68, v56, v65
	v_fmac_f32_e32 v59, v44, v63
	v_fmac_f32_e32 v68, v54, v66
	ds_read_b128 v[60:63], v19 offset:8496
	s_waitcnt lgkmcnt(2)
	v_fmac_f32_e32 v59, v53, v6
	v_fmac_f32_e32 v68, v52, v67
	v_fmac_f32_e32 v59, v43, v7
	v_pk_mul_f32 v[6:7], v[30:31], v[8:9]
	ds_read_b128 v[64:67], v19 offset:9520
	s_waitcnt lgkmcnt(2)
	v_fmac_f32_e32 v68, v45, v14
	v_add_f32_e32 v6, v59, v6
	v_fmac_f32_e32 v68, v46, v15
	v_add_f32_e32 v8, v6, v7
	v_pk_mul_f32 v[6:7], v[34:35], v[16:17]
	v_exp_f32_e32 v58, v58
	v_add_f32_e32 v6, v68, v6
	v_add_f32_e32 v9, v6, v7
	s_waitcnt lgkmcnt(1)
	v_pk_mul_f32 v[6:7], v[32:33], v[60:61]
	s_nop 0
	v_add_f32_e32 v6, v8, v6
	v_add_f32_e32 v8, v6, v7
	s_waitcnt lgkmcnt(0)
	v_pk_mul_f32 v[6:7], v[22:23], v[64:65]
	s_nop 0
	v_add_f32_e32 v6, v9, v6
	v_add_f32_e32 v9, v6, v7
	v_pk_mul_f32 v[6:7], v[20:21], v[62:63]
	s_nop 0
	v_add_f32_e32 v6, v8, v6
	v_add_f32_e32 v8, v6, v7
	v_pk_mul_f32 v[6:7], v[24:25], v[66:67]
	s_nop 0
	v_add_f32_e32 v6, v9, v6
	v_add_f32_e32 v6, v6, v7
	v_med3_f32 v6, v6, s5, v38
	v_mul_f32_e32 v6, 0x3fb8aa3b, v6
	v_exp_f32_e32 v59, v6
	v_med3_f32 v6, v8, s5, v38
	v_mul_f32_e32 v6, 0x3fb8aa3b, v6
	v_exp_f32_e32 v60, v6
	v_cvt_pk_bf16_f32 v6, v59, s0
	global_store_short v[28:29], v6, off offset:512
	ds_read_b128 v[6:9], v19 offset:8512
	ds_read_b128 v[14:17], v19 offset:9536
	ds_read_b128 v[62:65], v19 offset:8528
	ds_read_b128 v[66:69], v19 offset:8544
	ds_read_b128 v[70:73], v19 offset:8560
	ds_read_b128 v[74:77], v19 offset:9552
	s_waitcnt lgkmcnt(5)
	v_fma_f32 v61, v13, v6, v42
	s_waitcnt lgkmcnt(4)
	v_fma_f32 v78, v5, v14, v40
	v_fmac_f32_e32 v61, v10, v7
	v_fmac_f32_e32 v78, v11, v15
	v_fmac_f32_e32 v61, v2, v8
	v_fmac_f32_e32 v78, v4, v16
	v_fmac_f32_e32 v61, v3, v9
	v_fmac_f32_e32 v78, v12, v17
	ds_read_b128 v[6:9], v19 offset:9568
	s_waitcnt lgkmcnt(4)
	v_fmac_f32_e32 v61, v57, v62
	s_waitcnt lgkmcnt(1)
	v_fmac_f32_e32 v78, v51, v74
	v_fmac_f32_e32 v61, v49, v63
	v_fmac_f32_e32 v78, v56, v75
	v_fmac_f32_e32 v61, v50, v64
	v_fmac_f32_e32 v78, v54, v76
	v_fmac_f32_e32 v61, v44, v65
	v_fmac_f32_e32 v78, v52, v77
	v_fmac_f32_e32 v61, v53, v66
	s_waitcnt lgkmcnt(0)
	v_fmac_f32_e32 v78, v45, v6
	v_fmac_f32_e32 v61, v43, v67
	v_fmac_f32_e32 v78, v46, v7
	v_pk_mul_f32 v[6:7], v[30:31], v[68:69]
	ds_read_b128 v[14:17], v19 offset:9584
	v_add_f32_e32 v6, v61, v6
	v_add_f32_e32 v61, v6, v7
	v_pk_mul_f32 v[6:7], v[34:35], v[8:9]
	s_nop 0
	v_add_f32_e32 v6, v78, v6
	v_add_f32_e32 v8, v6, v7
	v_pk_mul_f32 v[6:7], v[32:33], v[70:71]
	s_nop 0
	v_add_f32_e32 v6, v61, v6
	v_add_f32_e32 v9, v6, v7
	s_waitcnt lgkmcnt(0)
	v_pk_mul_f32 v[6:7], v[22:23], v[14:15]
	s_nop 0
	v_add_f32_e32 v6, v8, v6
	v_add_f32_e32 v8, v6, v7
	v_pk_mul_f32 v[6:7], v[20:21], v[72:73]
	s_nop 0
	v_add_f32_e32 v6, v9, v6
	v_add_f32_e32 v9, v6, v7
	v_pk_mul_f32 v[6:7], v[24:25], v[16:17]
	s_nop 0
	v_add_f32_e32 v6, v8, v6
	v_add_f32_e32 v6, v6, v7
	v_med3_f32 v6, v6, s5, v38
	v_mul_f32_e32 v6, 0x3fb8aa3b, v6
	v_med3_f32 v7, v9, s5, v38
	v_exp_f32_e32 v61, v6
	v_mul_f32_e32 v62, 0x3fb8aa3b, v7
	ds_read_b128 v[6:9], v19 offset:8576
	ds_read_b128 v[14:17], v19 offset:9600
	ds_read_b128 v[64:67], v19 offset:8592
	ds_read_b128 v[68:71], v19 offset:9616
	v_cvt_pk_bf16_f32 v63, v61, s0
	global_store_short v[28:29], v63, off offset:640
	s_waitcnt lgkmcnt(3)
	v_fma_f32 v63, v13, v6, v42
	s_waitcnt lgkmcnt(2)
	v_fma_f32 v72, v5, v14, v40
	v_fmac_f32_e32 v63, v10, v7
	v_fmac_f32_e32 v72, v11, v15
	v_fmac_f32_e32 v63, v2, v8
	v_fmac_f32_e32 v72, v4, v16
	v_fmac_f32_e32 v63, v3, v9
	v_fmac_f32_e32 v72, v12, v17
	s_waitcnt lgkmcnt(1)
	v_fmac_f32_e32 v63, v57, v64
	ds_read_b128 v[6:9], v19 offset:8608
	ds_read_b128 v[14:17], v19 offset:9632
	v_fmac_f32_e32 v63, v49, v65
	s_waitcnt lgkmcnt(2)
	v_fmac_f32_e32 v72, v51, v68
	v_fmac_f32_e32 v63, v50, v66
	v_fmac_f32_e32 v72, v56, v69
	v_fmac_f32_e32 v63, v44, v67
	v_fmac_f32_e32 v72, v54, v70
	ds_read_b128 v[64:67], v19 offset:8624
	s_waitcnt lgkmcnt(2)
	v_fmac_f32_e32 v63, v53, v6
	v_fmac_f32_e32 v72, v52, v71
	v_fmac_f32_e32 v63, v43, v7
	v_pk_mul_f32 v[6:7], v[30:31], v[8:9]
	ds_read_b128 v[68:71], v19 offset:9648
	s_waitcnt lgkmcnt(2)
	v_fmac_f32_e32 v72, v45, v14
	v_add_f32_e32 v6, v63, v6
	v_fmac_f32_e32 v72, v46, v15
	v_add_f32_e32 v8, v6, v7
	v_pk_mul_f32 v[6:7], v[34:35], v[16:17]
	v_exp_f32_e32 v62, v62
	v_add_f32_e32 v6, v72, v6
	v_add_f32_e32 v9, v6, v7
	s_waitcnt lgkmcnt(1)
	v_pk_mul_f32 v[6:7], v[32:33], v[64:65]
	s_nop 0
	v_add_f32_e32 v6, v8, v6
	v_add_f32_e32 v8, v6, v7
	s_waitcnt lgkmcnt(0)
	v_pk_mul_f32 v[6:7], v[22:23], v[68:69]
	s_nop 0
	v_add_f32_e32 v6, v9, v6
	v_add_f32_e32 v9, v6, v7
	v_pk_mul_f32 v[6:7], v[20:21], v[66:67]
	s_nop 0
	v_add_f32_e32 v6, v8, v6
	v_add_f32_e32 v8, v6, v7
	v_pk_mul_f32 v[6:7], v[24:25], v[70:71]
	s_nop 0
	v_add_f32_e32 v6, v9, v6
	v_add_f32_e32 v6, v6, v7
	v_med3_f32 v6, v6, s5, v38
	v_mul_f32_e32 v6, 0x3fb8aa3b, v6
	v_exp_f32_e32 v63, v6
	v_med3_f32 v6, v8, s5, v38
	v_mul_f32_e32 v6, 0x3fb8aa3b, v6
	v_exp_f32_e32 v64, v6
	v_cvt_pk_bf16_f32 v6, v63, s0
	global_store_short v[28:29], v6, off offset:768
	ds_read_b128 v[6:9], v19 offset:8640
	ds_read_b128 v[14:17], v19 offset:9664
	ds_read_b128 v[66:69], v19 offset:8656
	ds_read_b128 v[70:73], v19 offset:8672
	ds_read_b128 v[74:77], v19 offset:8688
	ds_read_b128 v[78:81], v19 offset:9680
	s_waitcnt lgkmcnt(5)
	v_fma_f32 v65, v13, v6, v42
	s_waitcnt lgkmcnt(4)
	v_fma_f32 v82, v5, v14, v40
	v_fmac_f32_e32 v65, v10, v7
	v_fmac_f32_e32 v82, v11, v15
	v_fmac_f32_e32 v65, v2, v8
	v_fmac_f32_e32 v82, v4, v16
	v_fmac_f32_e32 v65, v3, v9
	v_fmac_f32_e32 v82, v12, v17
	ds_read_b128 v[6:9], v19 offset:9696
	s_waitcnt lgkmcnt(4)
	v_fmac_f32_e32 v65, v57, v66
	s_waitcnt lgkmcnt(1)
	v_fmac_f32_e32 v82, v51, v78
	v_fmac_f32_e32 v65, v49, v67
	v_fmac_f32_e32 v82, v56, v79
	v_fmac_f32_e32 v65, v50, v68
	v_fmac_f32_e32 v82, v54, v80
	v_fmac_f32_e32 v65, v44, v69
	v_fmac_f32_e32 v82, v52, v81
	v_fmac_f32_e32 v65, v53, v70
	s_waitcnt lgkmcnt(0)
	v_fmac_f32_e32 v82, v45, v6
	v_fmac_f32_e32 v65, v43, v71
	v_fmac_f32_e32 v82, v46, v7
	v_pk_mul_f32 v[6:7], v[30:31], v[72:73]
	ds_read_b128 v[14:17], v19 offset:9712
	v_add_f32_e32 v6, v65, v6
	v_add_f32_e32 v65, v6, v7
	v_pk_mul_f32 v[6:7], v[34:35], v[8:9]
	s_nop 0
	v_add_f32_e32 v6, v82, v6
	v_add_f32_e32 v8, v6, v7
	v_pk_mul_f32 v[6:7], v[32:33], v[74:75]
	s_nop 0
	v_add_f32_e32 v6, v65, v6
	v_add_f32_e32 v9, v6, v7
	s_waitcnt lgkmcnt(0)
	v_pk_mul_f32 v[6:7], v[22:23], v[14:15]
	s_nop 0
	v_add_f32_e32 v6, v8, v6
	v_add_f32_e32 v8, v6, v7
	v_pk_mul_f32 v[6:7], v[20:21], v[76:77]
	s_nop 0
	v_add_f32_e32 v6, v9, v6
	v_add_f32_e32 v9, v6, v7
	v_pk_mul_f32 v[6:7], v[24:25], v[16:17]
	s_nop 0
	v_add_f32_e32 v6, v8, v6
	v_add_f32_e32 v6, v6, v7
	v_med3_f32 v6, v6, s5, v38
	v_mul_f32_e32 v6, 0x3fb8aa3b, v6
	v_exp_f32_e32 v65, v6
	v_med3_f32 v6, v9, s5, v38
	v_mul_f32_e32 v6, 0x3fb8aa3b, v6
	v_exp_f32_e32 v66, v6
	v_cvt_pk_bf16_f32 v6, v65, s0
	global_store_short v[28:29], v6, off offset:896
	ds_read_b128 v[6:9], v19 offset:8704
	ds_read_b128 v[14:17], v19 offset:9728
	ds_read_b128 v[68:71], v19 offset:8720
	ds_read_b128 v[72:75], v19 offset:8736
	ds_read_b128 v[76:79], v19 offset:8752
	ds_read_b128 v[80:83], v19 offset:9744
	s_waitcnt lgkmcnt(5)
	v_fma_f32 v67, v13, v6, v42
	s_waitcnt lgkmcnt(4)
	v_fma_f32 v84, v5, v14, v40
	v_fmac_f32_e32 v67, v10, v7
	v_fmac_f32_e32 v84, v11, v15
	v_fmac_f32_e32 v67, v2, v8
	v_fmac_f32_e32 v84, v4, v16
	v_fmac_f32_e32 v67, v3, v9
	v_fmac_f32_e32 v84, v12, v17
	ds_read_b128 v[6:9], v19 offset:9760
	s_waitcnt lgkmcnt(4)
	v_fmac_f32_e32 v67, v57, v68
	s_waitcnt lgkmcnt(1)
	v_fmac_f32_e32 v84, v51, v80
	v_fmac_f32_e32 v67, v49, v69
	v_fmac_f32_e32 v84, v56, v81
	v_fmac_f32_e32 v67, v50, v70
	v_fmac_f32_e32 v84, v54, v82
	v_fmac_f32_e32 v67, v44, v71
	v_fmac_f32_e32 v84, v52, v83
	v_fmac_f32_e32 v67, v53, v72
	s_waitcnt lgkmcnt(0)
	v_fmac_f32_e32 v84, v45, v6
	v_fmac_f32_e32 v67, v43, v73
	v_fmac_f32_e32 v84, v46, v7
	v_pk_mul_f32 v[6:7], v[30:31], v[74:75]
	ds_read_b128 v[14:17], v19 offset:9776
	v_add_f32_e32 v6, v67, v6
	v_add_f32_e32 v67, v6, v7
	v_pk_mul_f32 v[6:7], v[34:35], v[8:9]
	s_nop 0
	v_add_f32_e32 v6, v84, v6
	v_add_f32_e32 v8, v6, v7
	v_pk_mul_f32 v[6:7], v[32:33], v[76:77]
	s_nop 0
	v_add_f32_e32 v6, v67, v6
	v_add_f32_e32 v9, v6, v7
	s_waitcnt lgkmcnt(0)
	v_pk_mul_f32 v[6:7], v[22:23], v[14:15]
	s_nop 0
	v_add_f32_e32 v6, v8, v6
	v_add_f32_e32 v8, v6, v7
	v_pk_mul_f32 v[6:7], v[20:21], v[78:79]
	s_nop 0
	v_add_f32_e32 v6, v9, v6
	v_add_f32_e32 v9, v6, v7
	v_pk_mul_f32 v[6:7], v[24:25], v[16:17]
	s_nop 0
	v_add_f32_e32 v6, v8, v6
	v_add_f32_e32 v6, v6, v7
	v_med3_f32 v6, v6, s5, v38
	v_mul_f32_e32 v6, 0x3fb8aa3b, v6
	v_exp_f32_e32 v67, v6
	v_med3_f32 v6, v9, s5, v38
	v_mul_f32_e32 v6, 0x3fb8aa3b, v6
	v_exp_f32_e32 v68, v6
	v_cvt_pk_bf16_f32 v6, v67, s0
	global_store_short v[28:29], v6, off offset:1024
	ds_read_b128 v[6:9], v19 offset:8768
	ds_read_b128 v[14:17], v19 offset:9792
	ds_read_b128 v[70:73], v19 offset:8784
	ds_read_b128 v[74:77], v19 offset:8800
	ds_read_b128 v[78:81], v19 offset:8816
	ds_read_b128 v[82:85], v19 offset:9808
	s_waitcnt lgkmcnt(5)
	v_fma_f32 v69, v13, v6, v42
	s_waitcnt lgkmcnt(4)
	v_fma_f32 v86, v5, v14, v40
	v_fmac_f32_e32 v69, v10, v7
	v_fmac_f32_e32 v86, v11, v15
	v_fmac_f32_e32 v69, v2, v8
	v_fmac_f32_e32 v86, v4, v16
	v_fmac_f32_e32 v69, v3, v9
	v_fmac_f32_e32 v86, v12, v17
	ds_read_b128 v[6:9], v19 offset:9824
	s_waitcnt lgkmcnt(4)
	v_fmac_f32_e32 v69, v57, v70
	s_waitcnt lgkmcnt(1)
	v_fmac_f32_e32 v86, v51, v82
	v_fmac_f32_e32 v69, v49, v71
	v_fmac_f32_e32 v86, v56, v83
	v_fmac_f32_e32 v69, v50, v72
	v_fmac_f32_e32 v86, v54, v84
	v_fmac_f32_e32 v69, v44, v73
	v_fmac_f32_e32 v86, v52, v85
	v_fmac_f32_e32 v69, v53, v74
	s_waitcnt lgkmcnt(0)
	v_fmac_f32_e32 v86, v45, v6
	v_fmac_f32_e32 v69, v43, v75
	v_fmac_f32_e32 v86, v46, v7
	v_pk_mul_f32 v[6:7], v[30:31], v[76:77]
	ds_read_b128 v[14:17], v19 offset:9840
	v_add_f32_e32 v6, v69, v6
	v_add_f32_e32 v69, v6, v7
	v_pk_mul_f32 v[6:7], v[34:35], v[8:9]
	ds_read_b128 v[72:75], v19 offset:8848
	v_add_f32_e32 v6, v86, v6
	v_add_f32_e32 v8, v6, v7
	v_pk_mul_f32 v[6:7], v[32:33], v[78:79]
	ds_read_b128 v[76:79], v19 offset:9872
	v_add_f32_e32 v6, v69, v6
	v_add_f32_e32 v9, v6, v7
	s_waitcnt lgkmcnt(2)
	v_pk_mul_f32 v[6:7], v[22:23], v[14:15]
	s_nop 0
	v_add_f32_e32 v6, v8, v6
	v_add_f32_e32 v8, v6, v7
	v_pk_mul_f32 v[6:7], v[20:21], v[80:81]
	s_nop 0
	v_add_f32_e32 v6, v9, v6
	v_add_f32_e32 v9, v6, v7
	v_pk_mul_f32 v[6:7], v[24:25], v[16:17]
	ds_read_b128 v[14:17], v19 offset:9856
	v_add_f32_e32 v6, v8, v6
	v_add_f32_e32 v6, v6, v7
	v_med3_f32 v6, v6, s5, v38
	v_mul_f32_e32 v6, 0x3fb8aa3b, v6
	v_exp_f32_e32 v69, v6
	v_med3_f32 v6, v9, s5, v38
	v_mul_f32_e32 v6, 0x3fb8aa3b, v6
	v_exp_f32_e32 v70, v6
	ds_read_b128 v[6:9], v19 offset:8832
	v_cvt_pk_bf16_f32 v71, v69, s0
	global_store_short v[28:29], v71, off offset:1152
	s_waitcnt lgkmcnt(1)
	v_fma_f32 v80, v5, v14, v40
	v_fmac_f32_e32 v80, v11, v15
	s_waitcnt lgkmcnt(0)
	v_fma_f32 v71, v13, v6, v42
	v_fmac_f32_e32 v71, v10, v7
	v_fmac_f32_e32 v71, v2, v8
	v_fmac_f32_e32 v71, v3, v9
	v_fmac_f32_e32 v71, v57, v72
	v_fmac_f32_e32 v80, v4, v16
	v_fmac_f32_e32 v71, v49, v73
	v_fmac_f32_e32 v80, v12, v17
	ds_read_b128 v[6:9], v19 offset:8864
	ds_read_b128 v[14:17], v19 offset:8880
	v_fmac_f32_e32 v71, v50, v74
	v_fmac_f32_e32 v71, v44, v75
	ds_read_b128 v[72:75], v19 offset:9888
	v_fmac_f32_e32 v80, v51, v76
	v_fmac_f32_e32 v80, v56, v77
	v_fmac_f32_e32 v80, v54, v78
	s_waitcnt lgkmcnt(2)
	v_fmac_f32_e32 v71, v53, v6
	v_fmac_f32_e32 v80, v52, v79
	v_fmac_f32_e32 v71, v43, v7
	v_pk_mul_f32 v[6:7], v[30:31], v[8:9]
	ds_read_b128 v[76:79], v19 offset:9904
	s_waitcnt lgkmcnt(1)
	v_fmac_f32_e32 v80, v45, v72
	v_add_f32_e32 v6, v71, v6
	v_fmac_f32_e32 v80, v46, v73
	v_add_f32_e32 v8, v6, v7
	v_pk_mul_f32 v[6:7], v[34:35], v[74:75]
	s_nop 0
	v_add_f32_e32 v6, v80, v6
	v_add_f32_e32 v9, v6, v7
	v_pk_mul_f32 v[6:7], v[32:33], v[14:15]
	s_nop 0
	v_add_f32_e32 v6, v8, v6
	v_add_f32_e32 v8, v6, v7
	s_waitcnt lgkmcnt(0)
	v_pk_mul_f32 v[6:7], v[22:23], v[76:77]
	ds_read_b128 v[74:77], v19 offset:8912
	v_add_f32_e32 v6, v9, v6
	v_add_f32_e32 v9, v6, v7
	v_pk_mul_f32 v[6:7], v[20:21], v[16:17]
	ds_read_b128 v[14:17], v19 offset:9920
	v_add_f32_e32 v6, v8, v6
	v_add_f32_e32 v8, v6, v7
	v_pk_mul_f32 v[6:7], v[24:25], v[78:79]
	ds_read_b128 v[78:81], v19 offset:9936
	v_add_f32_e32 v6, v9, v6
	v_add_f32_e32 v6, v6, v7
	v_med3_f32 v6, v6, s5, v38
	v_mul_f32_e32 v6, 0x3fb8aa3b, v6
	v_exp_f32_e32 v71, v6
	v_med3_f32 v6, v8, s5, v38
	v_mul_f32_e32 v6, 0x3fb8aa3b, v6
	v_exp_f32_e32 v72, v6
	ds_read_b128 v[6:9], v19 offset:8896
	v_cvt_pk_bf16_f32 v73, v71, s0
	global_store_short v[28:29], v73, off offset:1280
	s_waitcnt lgkmcnt(2)
	v_fma_f32 v82, v5, v14, v40
	v_fmac_f32_e32 v82, v11, v15
	s_waitcnt lgkmcnt(0)
	v_fma_f32 v73, v13, v6, v42
	v_fmac_f32_e32 v73, v10, v7
	v_fmac_f32_e32 v73, v2, v8
	v_fmac_f32_e32 v73, v3, v9
	v_fmac_f32_e32 v73, v57, v74
	v_fmac_f32_e32 v82, v4, v16
	v_fmac_f32_e32 v73, v49, v75
	v_fmac_f32_e32 v82, v12, v17
	ds_read_b128 v[6:9], v19 offset:8928
	ds_read_b128 v[14:17], v19 offset:8944
	v_fmac_f32_e32 v73, v50, v76
	v_fmac_f32_e32 v73, v44, v77
	ds_read_b128 v[74:77], v19 offset:9952
	v_fmac_f32_e32 v82, v51, v78
	v_fmac_f32_e32 v82, v56, v79
	v_fmac_f32_e32 v82, v54, v80
	s_waitcnt lgkmcnt(2)
	v_fmac_f32_e32 v73, v53, v6
	v_fmac_f32_e32 v82, v52, v81
	v_fmac_f32_e32 v73, v43, v7
	v_pk_mul_f32 v[6:7], v[30:31], v[8:9]
	ds_read_b128 v[78:81], v19 offset:9968
	s_waitcnt lgkmcnt(1)
	v_fmac_f32_e32 v82, v45, v74
	v_add_f32_e32 v6, v73, v6
	v_fmac_f32_e32 v82, v46, v75
	v_add_f32_e32 v8, v6, v7
	v_pk_mul_f32 v[6:7], v[34:35], v[76:77]
	s_nop 0
	v_add_f32_e32 v6, v82, v6
	v_add_f32_e32 v9, v6, v7
	v_pk_mul_f32 v[6:7], v[32:33], v[14:15]
	s_nop 0
	v_add_f32_e32 v6, v8, v6
	v_add_f32_e32 v8, v6, v7
	s_waitcnt lgkmcnt(0)
	v_pk_mul_f32 v[6:7], v[22:23], v[78:79]
	s_nop 0
	v_add_f32_e32 v6, v9, v6
	v_add_f32_e32 v9, v6, v7
	v_pk_mul_f32 v[6:7], v[20:21], v[16:17]
	s_nop 0
	v_add_f32_e32 v6, v8, v6
	v_add_f32_e32 v8, v6, v7
	v_pk_mul_f32 v[6:7], v[24:25], v[80:81]
	s_nop 0
	v_add_f32_e32 v6, v9, v6
	v_add_f32_e32 v6, v6, v7
	v_med3_f32 v6, v6, s5, v38
	v_med3_f32 v7, v8, s5, v38
	v_mul_f32_e32 v6, 0x3fb8aa3b, v6
	v_mul_f32_e32 v7, 0x3fb8aa3b, v7
	v_exp_f32_e32 v73, v6
	v_exp_f32_e32 v74, v7
	ds_read_b128 v[6:9], v19 offset:8960
	ds_read_b128 v[14:17], v19 offset:9984
	ds_read_b128 v[76:79], v19 offset:8976
	v_cvt_pk_bf16_f32 v75, v73, s0
	global_store_short v[28:29], v75, off offset:1408
	s_waitcnt lgkmcnt(2)
	v_fma_f32 v75, v13, v6, v42
	v_fmac_f32_e32 v75, v10, v7
	ds_read_b128 v[80:83], v19 offset:10000
	v_fmac_f32_e32 v75, v2, v8
	s_waitcnt lgkmcnt(2)
	v_fma_f32 v84, v5, v14, v40
	v_fmac_f32_e32 v75, v3, v9
	v_fmac_f32_e32 v84, v11, v15
	ds_read_b128 v[6:9], v19 offset:8992
	s_waitcnt lgkmcnt(2)
	v_fmac_f32_e32 v75, v57, v76
	v_fmac_f32_e32 v84, v4, v16
	v_fmac_f32_e32 v75, v49, v77
	v_fmac_f32_e32 v84, v12, v17
	v_fmac_f32_e32 v75, v50, v78
	ds_read_b128 v[14:17], v19 offset:10016
	v_fmac_f32_e32 v75, v44, v79
	ds_read_b128 v[76:79], v19 offset:9008
	s_waitcnt lgkmcnt(3)
	v_fmac_f32_e32 v84, v51, v80
	v_fmac_f32_e32 v84, v56, v81
	v_fmac_f32_e32 v84, v54, v82
	s_waitcnt lgkmcnt(2)
	v_fmac_f32_e32 v75, v53, v6
	v_fmac_f32_e32 v84, v52, v83
	v_fmac_f32_e32 v75, v43, v7
	v_pk_mul_f32 v[6:7], v[30:31], v[8:9]
	ds_read_b128 v[80:83], v19 offset:10032
	s_waitcnt lgkmcnt(2)
	v_fmac_f32_e32 v84, v45, v14
	v_add_f32_e32 v6, v75, v6
	v_fmac_f32_e32 v84, v46, v15
	v_add_f32_e32 v8, v6, v7
	v_pk_mul_f32 v[6:7], v[34:35], v[16:17]
	s_nop 0
	v_add_f32_e32 v6, v84, v6
	v_add_f32_e32 v9, v6, v7
	s_waitcnt lgkmcnt(1)
	v_pk_mul_f32 v[6:7], v[32:33], v[76:77]
	s_nop 0
	v_add_f32_e32 v6, v8, v6
	v_add_f32_e32 v8, v6, v7
	s_waitcnt lgkmcnt(0)
	v_pk_mul_f32 v[6:7], v[22:23], v[80:81]
	s_nop 0
	v_add_f32_e32 v6, v9, v6
	v_add_f32_e32 v9, v6, v7
	v_pk_mul_f32 v[6:7], v[20:21], v[78:79]
	s_nop 0
	v_add_f32_e32 v6, v8, v6
	v_add_f32_e32 v8, v6, v7
	v_pk_mul_f32 v[6:7], v[24:25], v[82:83]
	s_nop 0
	v_add_f32_e32 v6, v9, v6
	v_add_f32_e32 v6, v6, v7
	v_med3_f32 v6, v6, s5, v38
	v_med3_f32 v7, v8, s5, v38
	v_mul_f32_e32 v6, 0x3fb8aa3b, v6
	v_mul_f32_e32 v7, 0x3fb8aa3b, v7
	v_exp_f32_e32 v75, v6
	v_exp_f32_e32 v76, v7
	ds_read_b128 v[6:9], v19 offset:9024
	ds_read_b128 v[14:17], v19 offset:10048
	ds_read_b128 v[78:81], v19 offset:9040
	v_cvt_pk_bf16_f32 v77, v75, s0
	global_store_short v[28:29], v77, off offset:1536
	s_waitcnt lgkmcnt(2)
	v_fma_f32 v77, v13, v6, v42
	v_fmac_f32_e32 v77, v10, v7
	ds_read_b128 v[82:85], v19 offset:10064
	v_fmac_f32_e32 v77, v2, v8
	s_waitcnt lgkmcnt(2)
	v_fma_f32 v86, v5, v14, v40
	v_fmac_f32_e32 v77, v3, v9
	v_fmac_f32_e32 v86, v11, v15
	ds_read_b128 v[6:9], v19 offset:9056
	s_waitcnt lgkmcnt(2)
	v_fmac_f32_e32 v77, v57, v78
	v_fmac_f32_e32 v86, v4, v16
	v_fmac_f32_e32 v77, v49, v79
	v_fmac_f32_e32 v86, v12, v17
	v_fmac_f32_e32 v77, v50, v80
	ds_read_b128 v[14:17], v19 offset:10080
	v_fmac_f32_e32 v77, v44, v81
	ds_read_b128 v[78:81], v19 offset:9072
	s_waitcnt lgkmcnt(3)
	v_fmac_f32_e32 v86, v51, v82
	v_fmac_f32_e32 v86, v56, v83
	v_fmac_f32_e32 v86, v54, v84
	s_waitcnt lgkmcnt(2)
	v_fmac_f32_e32 v77, v53, v6
	v_fmac_f32_e32 v86, v52, v85
	v_fmac_f32_e32 v77, v43, v7
	v_pk_mul_f32 v[6:7], v[30:31], v[8:9]
	ds_read_b128 v[82:85], v19 offset:10096
	s_waitcnt lgkmcnt(2)
	v_fmac_f32_e32 v86, v45, v14
	v_add_f32_e32 v6, v77, v6
	v_fmac_f32_e32 v86, v46, v15
	v_add_f32_e32 v8, v6, v7
	v_pk_mul_f32 v[6:7], v[34:35], v[16:17]
	s_nop 0
	v_add_f32_e32 v6, v86, v6
	v_add_f32_e32 v9, v6, v7
	s_waitcnt lgkmcnt(1)
	v_pk_mul_f32 v[6:7], v[32:33], v[78:79]
	s_nop 0
	v_add_f32_e32 v6, v8, v6
	v_add_f32_e32 v8, v6, v7
	s_waitcnt lgkmcnt(0)
	v_pk_mul_f32 v[6:7], v[22:23], v[82:83]
	s_nop 0
	v_add_f32_e32 v6, v9, v6
	v_add_f32_e32 v9, v6, v7
	v_pk_mul_f32 v[6:7], v[20:21], v[80:81]
	s_nop 0
	v_add_f32_e32 v6, v8, v6
	v_add_f32_e32 v8, v6, v7
	v_pk_mul_f32 v[6:7], v[24:25], v[84:85]
	s_nop 0
	v_add_f32_e32 v6, v9, v6
	v_add_f32_e32 v6, v6, v7
	v_med3_f32 v6, v6, s5, v38
	v_mul_f32_e32 v6, 0x3fb8aa3b, v6
	v_med3_f32 v7, v8, s5, v38
	v_exp_f32_e32 v77, v6
	v_mul_f32_e32 v6, 0x3fb8aa3b, v7
	v_exp_f32_e32 v78, v6
	ds_read_b128 v[6:9], v19 offset:9088
	v_cvt_pk_bf16_f32 v14, v77, s0
	global_store_short v[28:29], v14, off offset:1664
	ds_read_b128 v[14:17], v19 offset:9104
	ds_read_b128 v[80:83], v19 offset:10112
	s_waitcnt lgkmcnt(2)
	v_fma_f32 v79, v13, v6, v42
	v_fmac_f32_e32 v79, v10, v7
	v_fmac_f32_e32 v79, v2, v8
	v_fmac_f32_e32 v79, v3, v9
	ds_read_b128 v[6:9], v19 offset:10128
	s_waitcnt lgkmcnt(1)
	v_fma_f32 v86, v5, v80, v40
	v_fmac_f32_e32 v86, v11, v81
	v_fmac_f32_e32 v79, v57, v14
	v_fmac_f32_e32 v86, v4, v82
	v_fmac_f32_e32 v79, v49, v15
	v_fmac_f32_e32 v86, v12, v83
	v_fmac_f32_e32 v79, v50, v16
	v_fmac_f32_e32 v79, v44, v17
	ds_read_b128 v[14:17], v19 offset:9120
	s_waitcnt lgkmcnt(1)
	v_fmac_f32_e32 v86, v51, v6
	v_fmac_f32_e32 v86, v56, v7
	v_fmac_f32_e32 v86, v54, v8
	v_fmac_f32_e32 v86, v52, v9
	ds_read_b128 v[6:9], v19 offset:10144
	ds_read_b128 v[80:83], v19 offset:9136
	s_waitcnt lgkmcnt(2)
	v_fmac_f32_e32 v79, v53, v14
	v_fmac_f32_e32 v79, v43, v15
	v_pk_mul_f32 v[84:85], v[30:31], v[16:17]
	ds_read_b128 v[14:17], v19 offset:10160
	s_waitcnt lgkmcnt(2)
	v_fmac_f32_e32 v86, v45, v6
	v_add_f32_e32 v6, v79, v84
	v_fmac_f32_e32 v86, v46, v7
	v_add_f32_e32 v79, v6, v85
	v_pk_mul_f32 v[6:7], v[34:35], v[8:9]
	s_nop 0
	v_add_f32_e32 v6, v86, v6
	v_add_f32_e32 v8, v6, v7
	s_waitcnt lgkmcnt(1)
	v_pk_mul_f32 v[6:7], v[32:33], v[80:81]
	ds_read_b128 v[86:89], v19 offset:10176
	v_add_f32_e32 v6, v79, v6
	v_add_f32_e32 v9, v6, v7
	s_waitcnt lgkmcnt(1)
	v_pk_mul_f32 v[6:7], v[22:23], v[14:15]
	s_waitcnt lgkmcnt(0)
	v_fmac_f32_e32 v40, v5, v86
	v_add_f32_e32 v6, v8, v6
	v_add_f32_e32 v8, v6, v7
	v_pk_mul_f32 v[6:7], v[20:21], v[82:83]
	ds_read_b128 v[82:85], v19 offset:9152
	v_add_f32_e32 v6, v9, v6
	v_add_f32_e32 v9, v6, v7
	v_pk_mul_f32 v[6:7], v[24:25], v[16:17]
	ds_read_b128 v[14:17], v19 offset:10192
	v_add_f32_e32 v6, v8, v6
	v_add_f32_e32 v6, v6, v7
	v_med3_f32 v6, v6, s5, v38
	v_mul_f32_e32 v6, 0x3fb8aa3b, v6
	v_exp_f32_e32 v79, v6
	v_med3_f32 v7, v9, s5, v38
	v_mul_f32_e32 v7, 0x3fb8aa3b, v7
	v_exp_f32_e32 v80, v7
	v_cvt_pk_bf16_f32 v6, v79, s0
	global_store_short v[28:29], v6, off offset:1792
	ds_read_b128 v[6:9], v19 offset:9168
	s_waitcnt lgkmcnt(2)
	v_fmac_f32_e32 v42, v13, v82
	v_fmac_f32_e32 v42, v10, v83
	v_fmac_f32_e32 v40, v11, v87
	v_fmac_f32_e32 v42, v2, v84
	v_fmac_f32_e32 v42, v3, v85
	v_fmac_f32_e32 v40, v4, v88
	v_fmac_f32_e32 v40, v12, v89
	ds_read_b128 v[10:13], v19 offset:9184
	ds_read_b128 v[2:5], v19 offset:9200
	s_waitcnt lgkmcnt(2)
	v_fmac_f32_e32 v42, v57, v6
	v_fmac_f32_e32 v42, v49, v7
	ds_read_b128 v[82:85], v19 offset:10208
	v_fmac_f32_e32 v40, v51, v14
	v_fmac_f32_e32 v42, v50, v8
	v_fmac_f32_e32 v40, v56, v15
	v_fmac_f32_e32 v42, v44, v9
	v_fmac_f32_e32 v40, v54, v16
	s_waitcnt lgkmcnt(2)
	v_fmac_f32_e32 v42, v53, v10
	ds_read_b128 v[6:9], v19 offset:10224
	v_fmac_f32_e32 v40, v52, v17
	v_fmac_f32_e32 v42, v43, v11
	v_pk_mul_f32 v[10:11], v[30:31], v[12:13]
	s_waitcnt lgkmcnt(1)
	v_fmac_f32_e32 v40, v45, v82
	v_add_f32_e32 v10, v42, v10
	v_fmac_f32_e32 v40, v46, v83
	v_add_f32_e32 v12, v10, v11
	v_pk_mul_f32 v[10:11], v[34:35], v[84:85]
	v_pk_mul_f32 v[2:3], v[32:33], v[2:3]
	v_add_f32_e32 v10, v40, v10
	v_add_f32_e32 v2, v12, v2
	v_add_f32_e32 v10, v10, v11
	v_add_f32_e32 v11, v2, v3
	s_waitcnt lgkmcnt(0)
	v_pk_mul_f32 v[2:3], v[22:23], v[6:7]
	s_nop 0
	v_add_f32_e32 v2, v10, v2
	v_add_f32_e32 v6, v2, v3
	v_pk_mul_f32 v[2:3], v[20:21], v[4:5]
	v_cvt_pk_bf16_f32 v5, v64, v66
	v_add_f32_e32 v2, v11, v2
	v_add_f32_e32 v4, v2, v3
	v_pk_mul_f32 v[2:3], v[24:25], v[8:9]
	s_nop 0
	v_add_f32_e32 v2, v6, v2
	v_add_f32_e32 v2, v2, v3
	v_med3_f32 v2, v2, s5, v38
	v_mul_f32_e32 v2, 0x3fb8aa3b, v2
	v_exp_f32_e32 v10, v2
	v_med3_f32 v2, v4, s5, v38
	v_mul_f32_e32 v2, 0x3fb8aa3b, v2
	v_exp_f32_e32 v11, v2
	v_cvt_pk_bf16_f32 v2, v10, s0
	global_store_short v[28:29], v2, off offset:1920
	v_lshlrev_b32_e32 v2, 7, v36
	v_or3_b32 v26, v2, s4, v26
	v_lshl_add_u64 v[6:7], s[12:13], 0, v[26:27]
	v_cvt_pk_bf16_f32 v2, v37, v41
	v_cvt_pk_bf16_f32 v3, v48, v58
	v_cvt_pk_bf16_f32 v4, v60, v62
	global_store_dwordx4 v[6:7], v[2:5], off
	v_lshl_add_u64 v[8:9], s[14:15], 0, v[26:27]
	s_mov_b64 s[4:5], 0
	v_cvt_pk_bf16_f32 v2, v68, v70
	v_cvt_pk_bf16_f32 v3, v72, v74
	v_cvt_pk_bf16_f32 v4, v76, v78
	v_cvt_pk_bf16_f32 v5, v80, v11
	global_store_dwordx4 v[6:7], v[2:5], off offset:16
	s_nop 1
	v_cvt_pk_bf16_f32 v2, v18, v39
	v_cvt_pk_bf16_f32 v3, v47, v55
	v_cvt_pk_bf16_f32 v4, v59, v61
	v_cvt_pk_bf16_f32 v5, v63, v65
	global_store_dwordx4 v[8:9], v[2:5], off
	s_nop 1
	v_cvt_pk_bf16_f32 v2, v67, v69
	v_cvt_pk_bf16_f32 v3, v71, v73
	v_cvt_pk_bf16_f32 v4, v75, v77
	v_cvt_pk_bf16_f32 v5, v79, v10
	global_store_dwordx4 v[8:9], v[2:5], off offset:16

.LBB13_17:
	s_cbranch_execnz .LBB13_2
.LBB13_18:
	s_endpgm

	.amdhsa_kernel _Z11prep_kernelPKfS0_S0_S0_S0_S0_S0_S0_S0_S0_S0_S0_PtS1_S1_S1_S1_S1_
		.amdhsa_group_segment_fixed_size 16640
		.amdhsa_private_segment_fixed_size 0
		.amdhsa_kernarg_size 144
		.amdhsa_user_sgpr_count 2
		.amdhsa_user_sgpr_dispatch_ptr 0
		.amdhsa_user_sgpr_queue_ptr 0
		.amdhsa_user_sgpr_kernarg_segment_ptr 1
		.amdhsa_user_sgpr_dispatch_id 0
		.amdhsa_user_sgpr_kernarg_preload_length 0
		.amdhsa_user_sgpr_kernarg_preload_offset 0
		.amdhsa_user_sgpr_private_segment_size 0
		.amdhsa_uses_dynamic_stack 0
		.amdhsa_enable_private_segment 0
		.amdhsa_system_sgpr_workgroup_id_x 1
		.amdhsa_system_sgpr_workgroup_id_y 0
		.amdhsa_system_sgpr_workgroup_id_z 0
		.amdhsa_system_sgpr_workgroup_info 0
		.amdhsa_system_vgpr_workitem_id 0
		.amdhsa_next_free_vgpr 124
		.amdhsa_next_free_sgpr 28
		.amdhsa_accum_offset 112
		.amdhsa_reserve_vcc 1
		.amdhsa_float_round_mode_32 0
		.amdhsa_float_round_mode_16_64 0
		.amdhsa_float_denorm_mode_32 3
		.amdhsa_float_denorm_mode_16_64 3
		.amdhsa_dx10_clamp 1
		.amdhsa_ieee_mode 1
		.amdhsa_fp16_overflow 0
		.amdhsa_tg_split 0
		.amdhsa_exception_fp_ieee_invalid_op 0
		.amdhsa_exception_fp_denorm_src 0
		.amdhsa_exception_fp_ieee_div_zero 0
		.amdhsa_exception_fp_ieee_overflow 0
		.amdhsa_exception_fp_ieee_underflow 0
		.amdhsa_exception_fp_ieee_inexact 0
		.amdhsa_exception_int_div_zero 0
	.end_amdhsa_kernel

amdhsa.kernels:
  - .agpr_count:     0
    .args:
      - .actual_access:  read_only
        .address_space:  global
        .offset:         0
        .size:           8
        .value_kind:     global_buffer
      - .actual_access:  read_only
        .address_space:  global
        .offset:         8
        .size:           8
        .value_kind:     global_buffer
      - .actual_access:  write_only
        .address_space:  global
        .offset:         16
        .size:           8
        .value_kind:     global_buffer
      - .offset:         24
        .size:           4
        .value_kind:     by_value
      - .offset:         28
        .size:           4
        .value_kind:     by_value
      - .offset:         32
        .size:           4
        .value_kind:     by_value
      - .offset:         36
        .size:           4
        .value_kind:     by_value
    .group_segment_fixed_size: 8256
    .kernarg_segment_align: 8
    .kernarg_segment_size: 40
    .language:       OpenCL C
    .language_version:
      - 2
      - 0
    .max_flat_workgroup_size: 256
    .name:           _Z14gemm_f32_naivePKfS0_Pfiiii
    .private_segment_fixed_size: 0
    .sgpr_count:     24
    .sgpr_spill_count: 0
    .symbol:         _Z14gemm_f32_naivePKfS0_Pfiiii.kd
    .uniform_work_group_size: 1
    .uses_dynamic_stack: false
    .vgpr_count:     76
    .vgpr_spill_count: 0
    .wavefront_size: 64
  - .agpr_count:     0
    .args:
      - .actual_access:  read_only
        .address_space:  global
        .offset:         0
        .size:           8
        .value_kind:     global_buffer
      - .actual_access:  write_only
        .address_space:  global
        .offset:         8
        .size:           8
        .value_kind:     global_buffer
      - .actual_access:  write_only
        .address_space:  global
        .offset:         16
        .size:           8
        .value_kind:     global_buffer
      - .actual_access:  write_only
        .address_space:  global
        .offset:         24
        .size:           8
        .value_kind:     global_buffer
      - .actual_access:  write_only
        .address_space:  global
        .offset:         32
        .size:           8
        .value_kind:     global_buffer
      - .actual_access:  write_only
        .address_space:  global
        .offset:         40
        .size:           8
        .value_kind:     global_buffer
      - .actual_access:  write_only
        .address_space:  global
        .offset:         48
        .size:           8
        .value_kind:     global_buffer
    .group_segment_fixed_size: 0
    .kernarg_segment_align: 8
    .kernarg_segment_size: 56
    .language:       OpenCL C
    .language_version:
      - 2
      - 0
    .max_flat_workgroup_size: 256
    .name:           _Z10post_naivePKfPtS1_S1_S1_S1_S1_
    .private_segment_fixed_size: 0
    .sgpr_count:     28
    .sgpr_spill_count: 0
    .symbol:         _Z10post_naivePKfPtS1_S1_S1_S1_S1_.kd
    .uniform_work_group_size: 1
    .uses_dynamic_stack: false
    .vgpr_count:     38
    .vgpr_spill_count: 0
    .wavefront_size: 64
  - .agpr_count:     0
    .args:
      - .actual_access:  read_only
        .address_space:  global
        .offset:         0
        .size:           8
        .value_kind:     global_buffer
      - .actual_access:  read_only
        .address_space:  global
        .offset:         8
        .size:           8
        .value_kind:     global_buffer
      - .actual_access:  read_only
        .address_space:  global
        .offset:         16
        .size:           8
        .value_kind:     global_buffer
      - .actual_access:  read_only
        .address_space:  global
        .offset:         24
        .size:           8
        .value_kind:     global_buffer
      - .actual_access:  read_only
        .address_space:  global
        .offset:         32
        .size:           8
        .value_kind:     global_buffer
      - .actual_access:  read_only
        .address_space:  global
        .offset:         40
        .size:           8
        .value_kind:     global_buffer
      - .actual_access:  read_only
        .address_space:  global
        .offset:         48
        .size:           8
        .value_kind:     global_buffer
      - .actual_access:  write_only
        .address_space:  global
        .offset:         56
        .size:           8
        .value_kind:     global_buffer
      - .actual_access:  write_only
        .address_space:  global
        .offset:         64
        .size:           8
        .value_kind:     global_buffer
      - .actual_access:  write_only
        .address_space:  global
        .offset:         72
        .size:           8
        .value_kind:     global_buffer
      - .actual_access:  write_only
        .address_space:  global
        .offset:         80
        .size:           8
        .value_kind:     global_buffer
    .group_segment_fixed_size: 1152
    .kernarg_segment_align: 8
    .kernarg_segment_size: 88
    .language:       OpenCL C
    .language_version:
      - 2
      - 0
    .max_flat_workgroup_size: 256
    .name:           _Z11gates_naivePKfS0_S0_S0_S0_S0_S0_PtS1_S1_S1_
    .private_segment_fixed_size: 0
    .sgpr_count:     32
    .sgpr_spill_count: 0
    .symbol:         _Z11gates_naivePKfS0_S0_S0_S0_S0_S0_PtS1_S1_S1_.kd
    .uniform_work_group_size: 1
    .uses_dynamic_stack: false
    .vgpr_count:     66
    .vgpr_spill_count: 0
    .wavefront_size: 64
  - .agpr_count:     0
    .args:
      - .actual_access:  read_only
        .address_space:  global
        .offset:         0
        .size:           8
        .value_kind:     global_buffer
      - .actual_access:  read_only
        .address_space:  global
        .offset:         8
        .size:           8
        .value_kind:     global_buffer
      - .actual_access:  read_only
        .address_space:  global
        .offset:         16
        .size:           8
        .value_kind:     global_buffer
      - .actual_access:  read_only
        .address_space:  global
        .offset:         24
        .size:           8
        .value_kind:     global_buffer
      - .actual_access:  read_only
        .address_space:  global
        .offset:         32
        .size:           8
        .value_kind:     global_buffer
      - .actual_access:  read_only
        .address_space:  global
        .offset:         40
        .size:           8
        .value_kind:     global_buffer
      - .actual_access:  read_only
        .address_space:  global
        .offset:         48
        .size:           8
        .value_kind:     global_buffer
      - .actual_access:  write_only
        .address_space:  global
        .offset:         56
        .size:           8
        .value_kind:     global_buffer
    .group_segment_fixed_size: 12560
    .kernarg_segment_align: 8
    .kernarg_segment_size: 64
    .language:       OpenCL C
    .language_version:
      - 2
      - 0
    .max_flat_workgroup_size: 256
    .name:           _Z10attn_naivePKtS0_S0_S0_S0_S0_PKfPf
    .private_segment_fixed_size: 0
    .sgpr_count:     33
    .sgpr_spill_count: 0
    .symbol:         _Z10attn_naivePKtS0_S0_S0_S0_S0_PKfPf.kd
    .uniform_work_group_size: 1
    .uses_dynamic_stack: false
    .vgpr_count:     82
    .vgpr_spill_count: 0
    .wavefront_size: 64
  - .agpr_count:     0
    .args:
      - .address_space:  global
        .offset:         0
        .size:           8
        .value_kind:     global_buffer
      - .address_space:  global
        .offset:         8
        .size:           8
        .value_kind:     global_buffer
      - .actual_access:  write_only
        .address_space:  global
        .offset:         16
        .size:           8
        .value_kind:     global_buffer
    .group_segment_fixed_size: 0
    .kernarg_segment_align: 8
    .kernarg_segment_size: 24
    .language:       OpenCL C
    .language_version:
      - 2
      - 0
    .max_flat_workgroup_size: 512
    .name:           _Z8gemm_outPKtS0_Pf
    .private_segment_fixed_size: 0
    .sgpr_count:     26
    .sgpr_spill_count: 0
    .symbol:         _Z8gemm_outPKtS0_Pf.kd
    .uniform_work_group_size: 1
    .uses_dynamic_stack: false
    .vgpr_count:     158
    .vgpr_spill_count: 0
    .wavefront_size: 64
  - .agpr_count:     0
    .args:
      - .address_space:  global
        .offset:         0
        .size:           8
        .value_kind:     global_buffer
      - .address_space:  global
        .offset:         8
        .size:           8
        .value_kind:     global_buffer
      - .actual_access:  write_only
        .address_space:  global
        .offset:         16
        .size:           8
        .value_kind:     global_buffer
    .group_segment_fixed_size: 0
    .kernarg_segment_align: 8
    .kernarg_segment_size: 24
    .language:       OpenCL C
    .language_version:
      - 2
      - 0
    .max_flat_workgroup_size: 512
    .name:           _Z9gemm_out2PKtS0_Pf
    .private_segment_fixed_size: 0
    .sgpr_count:     27
    .sgpr_spill_count: 0
    .symbol:         _Z9gemm_out2PKtS0_Pf.kd
    .uniform_work_group_size: 1
    .uses_dynamic_stack: false
    .vgpr_count:     146
    .vgpr_spill_count: 0
    .wavefront_size: 64
  - .agpr_count:     0
    .args:
      - .actual_access:  read_only
        .address_space:  global
        .offset:         0
        .size:           8
        .value_kind:     global_buffer
      - .actual_access:  write_only
        .address_space:  global
        .offset:         8
        .size:           8
        .value_kind:     global_buffer
    .group_segment_fixed_size: 0
    .kernarg_segment_align: 8
    .kernarg_segment_size: 16
    .language:       OpenCL C
    .language_version:
      - 2
      - 0
    .max_flat_workgroup_size: 256
    .name:           _Z6conv_xPKfPt
    .private_segment_fixed_size: 0
    .sgpr_count:     14
    .sgpr_spill_count: 0
    .symbol:         _Z6conv_xPKfPt.kd
    .uniform_work_group_size: 1
    .uses_dynamic_stack: false
    .vgpr_count:     12
    .vgpr_spill_count: 0
    .wavefront_size: 64
  - .agpr_count:     0
    .args:
      - .actual_access:  read_only
        .address_space:  global
        .offset:         0
        .size:           8
        .value_kind:     global_buffer
      - .actual_access:  read_only
        .address_space:  global
        .offset:         8
        .size:           8
        .value_kind:     global_buffer
      - .actual_access:  read_only
        .address_space:  global
        .offset:         16
        .size:           8
        .value_kind:     global_buffer
      - .actual_access:  read_only
        .address_space:  global
        .offset:         24
        .size:           8
        .value_kind:     global_buffer
      - .actual_access:  read_only
        .address_space:  global
        .offset:         32
        .size:           8
        .value_kind:     global_buffer
      - .actual_access:  write_only
        .address_space:  global
        .offset:         40
        .size:           8
        .value_kind:     global_buffer
      - .actual_access:  write_only
        .address_space:  global
        .offset:         48
        .size:           8
        .value_kind:     global_buffer
    .group_segment_fixed_size: 16640
    .kernarg_segment_align: 8
    .kernarg_segment_size: 56
    .language:       OpenCL C
    .language_version:
      - 2
      - 0
    .max_flat_workgroup_size: 256
    .name:           _Z7conv_wTPKfS0_S0_S0_S0_PtS1_
    .private_segment_fixed_size: 0
    .sgpr_count:     26
    .sgpr_spill_count: 0
    .symbol:         _Z7conv_wTPKfS0_S0_S0_S0_PtS1_.kd
    .uniform_work_group_size: 1
    .uses_dynamic_stack: false
    .vgpr_count:     51
    .vgpr_spill_count: 0
    .wavefront_size: 64
  - .agpr_count:     0
    .args:
      - .actual_access:  read_only
        .address_space:  global
        .offset:         0
        .size:           8
        .value_kind:     global_buffer
      - .actual_access:  read_only
        .address_space:  global
        .offset:         8
        .size:           8
        .value_kind:     global_buffer
      - .actual_access:  write_only
        .address_space:  global
        .offset:         16
        .size:           8
        .value_kind:     global_buffer
    .group_segment_fixed_size: 0
    .kernarg_segment_align: 8
    .kernarg_segment_size: 24
    .language:       OpenCL C
    .language_version:
      - 2
      - 0
    .max_flat_workgroup_size: 256
    .name:           _Z7conv_w1PKfS0_Pt
    .private_segment_fixed_size: 0
    .sgpr_count:     16
    .sgpr_spill_count: 0
    .symbol:         _Z7conv_w1PKfS0_Pt.kd
    .uniform_work_group_size: 1
    .uses_dynamic_stack: false
    .vgpr_count:     6
    .vgpr_spill_count: 0
    .wavefront_size: 64
  - .agpr_count:     8
    .args:
      - .actual_access:  read_only
        .address_space:  global
        .offset:         0
        .size:           8
        .value_kind:     global_buffer
      - .actual_access:  read_only
        .address_space:  global
        .offset:         8
        .size:           8
        .value_kind:     global_buffer
      - .actual_access:  read_only
        .address_space:  global
        .offset:         16
        .size:           8
        .value_kind:     global_buffer
      - .actual_access:  read_only
        .address_space:  global
        .offset:         24
        .size:           8
        .value_kind:     global_buffer
      - .actual_access:  read_only
        .address_space:  global
        .offset:         32
        .size:           8
        .value_kind:     global_buffer
      - .actual_access:  read_only
        .address_space:  global
        .offset:         40
        .size:           8
        .value_kind:     global_buffer
      - .actual_access:  write_only
        .address_space:  global
        .offset:         48
        .size:           8
        .value_kind:     global_buffer
      - .actual_access:  write_only
        .address_space:  global
        .offset:         56
        .size:           8
        .value_kind:     global_buffer
      - .actual_access:  write_only
        .address_space:  global
        .offset:         64
        .size:           8
        .value_kind:     global_buffer
    .group_segment_fixed_size: 10240
    .kernarg_segment_align: 8
    .kernarg_segment_size: 72
    .language:       OpenCL C
    .language_version:
      - 2
      - 0
    .max_flat_workgroup_size: 256
    .name:           _Z10gates_fastPKtS0_PKfS2_S2_S2_PtS3_S3_
    .private_segment_fixed_size: 0
    .sgpr_count:     24
    .sgpr_spill_count: 0
    .symbol:         _Z10gates_fastPKtS0_PKfS2_S2_S2_PtS3_S3_.kd
    .uniform_work_group_size: 1
    .uses_dynamic_stack: false
    .vgpr_count:     96
    .vgpr_spill_count: 0
    .wavefront_size: 64
  - .agpr_count:     4
    .args:
      - .actual_access:  read_only
        .address_space:  global
        .offset:         0
        .size:           8
        .value_kind:     global_buffer
      - .actual_access:  read_only
        .address_space:  global
        .offset:         8
        .size:           8
        .value_kind:     global_buffer
      - .actual_access:  read_only
        .address_space:  global
        .offset:         16
        .size:           8
        .value_kind:     global_buffer
      - .actual_access:  read_only
        .address_space:  global
        .offset:         24
        .size:           8
        .value_kind:     global_buffer
      - .actual_access:  write_only
        .address_space:  global
        .offset:         32
        .size:           8
        .value_kind:     global_buffer
      - .actual_access:  write_only
        .address_space:  global
        .offset:         40
        .size:           8
        .value_kind:     global_buffer
      - .actual_access:  write_only
        .address_space:  global
        .offset:         48
        .size:           8
        .value_kind:     global_buffer
    .group_segment_fixed_size: 0
    .kernarg_segment_align: 8
    .kernarg_segment_size: 56
    .language:       OpenCL C
    .language_version:
      - 2
      - 0
    .max_flat_workgroup_size: 256
    .name:           _Z10state_fastPKtS0_S0_S0_PtS1_Pf
    .private_segment_fixed_size: 0
    .sgpr_count:     20
    .sgpr_spill_count: 0
    .symbol:         _Z10state_fastPKtS0_S0_S0_PtS1_Pf.kd
    .uniform_work_group_size: 1
    .uses_dynamic_stack: false
    .vgpr_count:     184
    .vgpr_spill_count: 0
    .wavefront_size: 64
  - .agpr_count:     0
    .args:
      - .actual_access:  read_only
        .address_space:  global
        .offset:         0
        .size:           8
        .value_kind:     global_buffer
      - .actual_access:  read_only
        .address_space:  global
        .offset:         8
        .size:           8
        .value_kind:     global_buffer
      - .actual_access:  read_only
        .address_space:  global
        .offset:         16
        .size:           8
        .value_kind:     global_buffer
      - .actual_access:  write_only
        .address_space:  global
        .offset:         24
        .size:           8
        .value_kind:     global_buffer
      - .actual_access:  write_only
        .address_space:  global
        .offset:         32
        .size:           8
        .value_kind:     global_buffer
      - .actual_access:  write_only
        .address_space:  global
        .offset:         40
        .size:           8
        .value_kind:     global_buffer
    .group_segment_fixed_size: 0
    .kernarg_segment_align: 8
    .kernarg_segment_size: 48
    .language:       OpenCL C
    .language_version:
      - 2
      - 0
    .max_flat_workgroup_size: 256
    .name:           _Z11prefix_fastPKtS0_PKfPtS3_Pf
    .private_segment_fixed_size: 0
    .sgpr_count:     106
    .sgpr_spill_count: 41
    .symbol:         _Z11prefix_fastPKtS0_PKfPtS3_Pf.kd
    .uniform_work_group_size: 1
    .uses_dynamic_stack: false
    .vgpr_count:     205
    .vgpr_spill_count: 0
    .wavefront_size: 64
  - .agpr_count:     0
    .args:
      - .address_space:  global
        .offset:         0
        .size:           8
        .value_kind:     global_buffer
      - .address_space:  global
        .offset:         8
        .size:           8
        .value_kind:     global_buffer
      - .address_space:  global
        .offset:         16
        .size:           8
        .value_kind:     global_buffer
      - .actual_access:  read_only
        .address_space:  global
        .offset:         24
        .size:           8
        .value_kind:     global_buffer
      - .address_space:  global
        .offset:         32
        .size:           8
        .value_kind:     global_buffer
      - .address_space:  global
        .offset:         40
        .size:           8
        .value_kind:     global_buffer
      - .address_space:  global
        .offset:         48
        .size:           8
        .value_kind:     global_buffer
      - .address_space:  global
        .offset:         56
        .size:           8
        .value_kind:     global_buffer
      - .address_space:  global
        .offset:         64
        .size:           8
        .value_kind:     global_buffer
      - .address_space:  global
        .offset:         72
        .size:           8
        .value_kind:     global_buffer
      - .address_space:  global
        .offset:         80
        .size:           8
        .value_kind:     global_buffer
      - .actual_access:  write_only
        .address_space:  global
        .offset:         88
        .size:           8
        .value_kind:     global_buffer
    .group_segment_fixed_size: 0
    .kernarg_segment_align: 8
    .kernarg_segment_size: 96
    .language:       OpenCL C
    .language_version:
      - 2
      - 0
    .max_flat_workgroup_size: 512
    .name:           _Z9attn_fastPKtS0_S0_S0_S0_S0_S0_S0_S0_PKfS2_Pt
    .private_segment_fixed_size: 0
    .sgpr_count:     50
    .sgpr_spill_count: 0
    .symbol:         _Z9attn_fastPKtS0_S0_S0_S0_S0_S0_S0_S0_PKfS2_Pt.kd
    .uniform_work_group_size: 1
    .uses_dynamic_stack: false
    .vgpr_count:     152
    .vgpr_spill_count: 0
    .wavefront_size: 64
  - .agpr_count:     12
    .args:
      - .actual_access:  read_only
        .address_space:  global
        .offset:         0
        .size:           8
        .value_kind:     global_buffer
      - .actual_access:  read_only
        .address_space:  global
        .offset:         8
        .size:           8
        .value_kind:     global_buffer
      - .actual_access:  read_only
        .address_space:  global
        .offset:         16
        .size:           8
        .value_kind:     global_buffer
      - .actual_access:  read_only
        .address_space:  global
        .offset:         24
        .size:           8
        .value_kind:     global_buffer
      - .actual_access:  read_only
        .address_space:  global
        .offset:         32
        .size:           8
        .value_kind:     global_buffer
      - .actual_access:  read_only
        .address_space:  global
        .offset:         40
        .size:           8
        .value_kind:     global_buffer
      - .actual_access:  read_only
        .address_space:  global
        .offset:         48
        .size:           8
        .value_kind:     global_buffer
      - .actual_access:  read_only
        .address_space:  global
        .offset:         56
        .size:           8
        .value_kind:     global_buffer
      - .actual_access:  read_only
        .address_space:  global
        .offset:         64
        .size:           8
        .value_kind:     global_buffer
      - .actual_access:  read_only
        .address_space:  global
        .offset:         72
        .size:           8
        .value_kind:     global_buffer
      - .actual_access:  read_only
        .address_space:  global
        .offset:         80
        .size:           8
        .value_kind:     global_buffer
      - .actual_access:  read_only
        .address_space:  global
        .offset:         88
        .size:           8
        .value_kind:     global_buffer
      - .actual_access:  write_only
        .address_space:  global
        .offset:         96
        .size:           8
        .value_kind:     global_buffer
      - .actual_access:  write_only
        .address_space:  global
        .offset:         104
        .size:           8
        .value_kind:     global_buffer
      - .actual_access:  write_only
        .address_space:  global
        .offset:         112
        .size:           8
        .value_kind:     global_buffer
      - .actual_access:  write_only
        .address_space:  global
        .offset:         120
        .size:           8
        .value_kind:     global_buffer
      - .actual_access:  write_only
        .address_space:  global
        .offset:         128
        .size:           8
        .value_kind:     global_buffer
      - .actual_access:  write_only
        .address_space:  global
        .offset:         136
        .size:           8
        .value_kind:     global_buffer
    .group_segment_fixed_size: 16640
    .kernarg_segment_align: 8
    .kernarg_segment_size: 144
    .language:       OpenCL C
    .language_version:
      - 2
      - 0
    .max_flat_workgroup_size: 256
    .name:           _Z11prep_kernelPKfS0_S0_S0_S0_S0_S0_S0_S0_S0_S0_S0_PtS1_S1_S1_S1_S1_
    .private_segment_fixed_size: 0
    .sgpr_count:     34
    .sgpr_spill_count: 0
    .symbol:         _Z11prep_kernelPKfS0_S0_S0_S0_S0_S0_S0_S0_S0_S0_S0_PtS1_S1_S1_S1_S1_.kd
    .uniform_work_group_size: 1
    .uses_dynamic_stack: false
    .vgpr_count:     124
    .vgpr_spill_count: 0
    .wavefront_size: 64
  - .agpr_count:     0
    .args:
      - .address_space:  global
        .offset:         0
        .size:           8
        .value_kind:     global_buffer
      - .address_space:  global
        .offset:         8
        .size:           8
        .value_kind:     global_buffer
      - .offset:         16
        .size:           4
        .value_kind:     by_value
      - .offset:         20
        .size:           4
        .value_kind:     by_value
      - .offset:         24
        .size:           4
        .value_kind:     by_value
      - .offset:         28
        .size:           4
        .value_kind:     by_value
      - .address_space:  global
        .offset:         32
        .size:           8
        .value_kind:     global_buffer
    .group_segment_fixed_size: 0
    .kernarg_segment_align: 8
    .kernarg_segment_size: 40
    .language:       OpenCL C
    .language_version:
      - 2
      - 0
    .max_flat_workgroup_size: 1024
    .name:           _Z9dbg_cmp16PKtS0_iiffPf
    .private_segment_fixed_size: 0
    .sgpr_count:     18
    .sgpr_spill_count: 0
    .symbol:         _Z9dbg_cmp16PKtS0_iiffPf.kd
    .uniform_work_group_size: 1
    .uses_dynamic_stack: false
    .vgpr_count:     5
    .vgpr_spill_count: 0
    .wavefront_size: 64
  - .agpr_count:     0
    .args:
      - .address_space:  global
        .offset:         0
        .size:           8
        .value_kind:     global_buffer
      - .address_space:  global
        .offset:         8
        .size:           8
        .value_kind:     global_buffer
      - .offset:         16
        .size:           4
        .value_kind:     by_value
      - .offset:         20
        .size:           4
        .value_kind:     by_value
      - .offset:         24
        .size:           56
        .value_kind:     by_value
    .group_segment_fixed_size: 0
    .kernarg_segment_align: 8
    .kernarg_segment_size: 80
    .language:       OpenCL C
    .language_version:
      - 2
      - 0
    .max_flat_workgroup_size: 512
    .name:           _Z5gemm8ILi0EEvPKtS1_ii7EpiArgs
    .private_segment_fixed_size: 0
    .sgpr_count:     36
    .sgpr_spill_count: 0
    .symbol:         _Z5gemm8ILi0EEvPKtS1_ii7EpiArgs.kd
    .uniform_work_group_size: 1
    .uses_dynamic_stack: false
    .vgpr_count:     246
    .vgpr_spill_count: 0
    .wavefront_size: 64
  - .agpr_count:     0
    .args:
      - .address_space:  global
        .offset:         0
        .size:           8
        .value_kind:     global_buffer
      - .address_space:  global
        .offset:         8
        .size:           8
        .value_kind:     global_buffer
      - .address_space:  global
        .offset:         16
        .size:           8
        .value_kind:     global_buffer
      - .address_space:  global
        .offset:         24
        .size:           8
        .value_kind:     global_buffer
      - .actual_access:  write_only
        .address_space:  global
        .offset:         32
        .size:           8
        .value_kind:     global_buffer
      - .actual_access:  write_only
        .address_space:  global
        .offset:         40
        .size:           8
        .value_kind:     global_buffer
      - .actual_access:  write_only
        .address_space:  global
        .offset:         48
        .size:           8
        .value_kind:     global_buffer
    .group_segment_fixed_size: 81920
    .kernarg_segment_align: 8
    .kernarg_segment_size: 56
    .language:       OpenCL C
    .language_version:
      - 2
      - 0
    .max_flat_workgroup_size: 256
    .name:           _Z9scan_fastILb1EEvPKtS1_S1_S1_PtS2_Pf
    .private_segment_fixed_size: 0
    .sgpr_count:     62
    .sgpr_spill_count: 0
    .symbol:         _Z9scan_fastILb1EEvPKtS1_S1_S1_PtS2_Pf.kd
    .uniform_work_group_size: 1
    .uses_dynamic_stack: false
    .vgpr_count:     160
    .vgpr_spill_count: 0
    .wavefront_size: 64
